# EpiGU (P7/P16): row-scale quad loads prefetched in the peeled first K iteration into free VGPRs v220-251; epilogue vmcnt(0) wait and address VALU removed
# speedup vs baseline: 1.0087x; 1.0008x over previous
; #define PG8_STAGE(bufoff, gbase, voff) do { _Pragma("unroll") for (int _i = 0; _i < 2; ++_i) \
;         __builtin_amdgcn_global_load_lds((const unsigned*)((const char*)(gbase) + (voff)[_i]), (PG8_LAS unsigned*)(lds + (bufoff) + ldsw + _i * 8192), 16, 0, 0); } while (0)
; #define PG8_LDA(dst, b, h) do { _Pragma("unroll") for (int m = 0; m < 4; ++m) _Pragma("unroll") for (int k = 0; k < 2; ++k) dst[m][k] = *(const PG8_LAS bf16x8*)(lds + PG8_SA(b, h) + aoff + m * 2048 + k * 1024); } while (0)
; #define PG8_LDB(dst, b, h) do { _Pragma("unroll") for (int n = 0; n < 2; ++n) _Pragma("unroll") for (int k = 0; k < 2; ++k) dst[n][k] = *(const PG8_LAS bf16x8*)(lds + PG8_SB(b, h) + boff + n * 2048 + k * 1024); } while (0)
; #define PG8_WAIT_V(n) asm volatile("s_waitcnt vmcnt(" #n ")" ::: "memory")
; #define PG8_BAR __builtin_amdgcn_s_barrier()
;     __device__ __forceinline__ void operator()(const f32x4 (&acc)[2][2][4][2], const Unit& u, int wr, int wc, int fr, int fq) const {
;     ...
;             f32x4 qd[2][4];
; #pragma unroll
;             for (int ai = 0; ai < 2; ++ai)
; #pragma unroll
;                 for (int m = 0; m < 4; ++m) qd[ai][m] = row_quad(ssq, u.pm * BM + ai * HALF + wr * 64 + m * 16 + fr, fq);
; template <class Epi, class Sched, bool ALIGN_EPI = false, bool SP2 = false>
; __device__ __forceinline__ void gemm_phase(PG8_LAS unsigned char* lds, const Gemm g, const Sched& S, const Epi& E, const int wid) {
;     ...
;         for (int t = 0; t < nt; t += 2) {
;             const bool last = (t == nt - 2);
;             const char* a1 = cA + (size_t)(t + 1) * kstep;
;             const char* a2 = last ? nA : cA + (size_t)(t + 2) * kstep; const char* b2 = last ? nB : cB + (size_t)(t + 2) * kstep;
;             const char* a3 = a2 + kstep; const char* b3 = b2 + kstep;
;             if (last && has_next) S.a_ready(nxt);
;             if constexpr (SP2) {
;             PG8_LDB(B0, 0, 0); PG8_LDB(B1, 0, 1); PG8_SCHED; PG8_LDA(At, 0, 0); PG8_STAGE(PG8_SA(1, 1), a1 + hstepA, voffA);
;             PG8_WAIT_V(8); PG8_WAIT_L(0); PG8_BAR; PG8_MMA(0, 0, At, B0); PG8_MMA(0, 1, At, B1); PG8_BAR; PG8_SCHED;
;             PG8_LDA(At, 0, 1); PG8_STAGE(PG8_SB(0, 0), b2, voffB); PG8_STAGE(PG8_SB(0, 1), b2 + hstepB, voffB); PG8_STAGE(PG8_SA(0, 0), a2, voffA);
;             PG8_WAIT_V(8); PG8_WAIT_L(0); PG8_BAR; PG8_MMA(1, 0, At, B0); PG8_MMA(1, 1, At, B1); PG8_BAR; PG8_SCHED;
.LBB0_1866:
	s_ashr_i32 s17, s16, 31
	s_lshl_b64 s[18:19], s[16:17], 19
	s_add_u32 s18, s0, s18
	s_addc_u32 s19, s1, s19
	s_and_b64 s[20:21], s[2:3], exec
	s_cselect_b32 s17, s19, s25
	s_cselect_b32 s49, s18, s24
	s_ashr_i32 s15, s14, 31
	s_lshl_b64 s[20:21], s[14:15], 19
	s_add_u32 s20, s30, s20
	s_addc_u32 s21, s31, s21
	s_and_b64 s[28:29], s[2:3], exec
	s_cselect_b32 s15, s21, s27
	s_cselect_b32 s64, s20, s26
	s_add_u32 s24, s24, 0x40080
	s_addc_u32 s25, s25, 0
	s_add_u32 s65, s26, 0x100
	s_addc_u32 s66, s27, 0
	s_mov_b32 s67, -2
	v_add_u32_e32 v252, 0x18000, v165
	v_add_u32_e32 v253, 0x1c000, v165
	ds_read_b128 v[148:151], v166
	ds_read_b128 v[152:155], v166 offset:1024
	ds_read_b128 v[156:159], v166 offset:2048
	ds_read_b128 v[160:163], v166 offset:3072
	ds_read_b128 v[172:175], v167
	ds_read_b128 v[176:179], v167 offset:1024
	ds_read_b128 v[180:183], v167 offset:2048
	ds_read_b128 v[184:187], v167 offset:3072
	s_add_u32 s26, s24, 0xfffc0080
	s_addc_u32 s27, s25, -1
	s_cmp_eq_u32 s67, 12
	s_cselect_b32 s29, s17, s27
	s_cselect_b32 s28, s49, s26
	s_cselect_b32 s27, s15, s66
	s_cselect_b32 s26, s64, s65
	s_add_i32 m0, s36, 0xc000
	ds_read_b128 v[188:191], v168
	ds_read_b128 v[192:195], v168 offset:1024
	ds_read_b128 v[196:199], v168 offset:2048
	ds_read_b128 v[200:203], v168 offset:3072
	ds_read_b128 v[204:207], v168 offset:4096
	ds_read_b128 v[208:211], v168 offset:5120
	ds_read_b128 v[212:215], v168 offset:6144
	ds_read_b128 v[216:219], v168 offset:7168
	global_load_lds_dwordx4 v140, s[24:25]
	s_add_i32 m0, s36, 0xe000
	s_nop 0
	global_load_lds_dwordx4 v142, s[24:25]
	s_waitcnt vmcnt(8) lgkmcnt(0)
	v_lshl_add_u32 v220, s22, 8, v164
	v_add_u32_e32 v236, 0x80, v220
	v_ashrrev_i32_e32 v221, 31, v220
	v_ashrrev_i32_e32 v237, 31, v236
	v_lshlrev_b64 v[220:221], 6, v[220:221]
	v_lshlrev_b64 v[236:237], 6, v[236:237]
	v_lshl_add_u64 v[220:221], v[138:139], 0, v[220:221]
	v_lshl_add_u64 v[236:237], v[138:139], 0, v[236:237]
	global_load_dwordx4 v[224:227], v[220:221], off offset:1024
	global_load_dwordx4 v[228:231], v[220:221], off offset:2048
	global_load_dwordx4 v[232:235], v[220:221], off offset:3072
	global_load_dwordx4 v[240:243], v[236:237], off offset:1024
	global_load_dwordx4 v[244:247], v[236:237], off offset:2048
	global_load_dwordx4 v[248:251], v[236:237], off offset:3072
	s_nop 0
	global_load_dwordx4 v[220:223], v[220:221], off
	s_nop 0
	global_load_dwordx4 v[236:239], v[236:237], off
	s_barrier
	s_setprio 1
	v_mfma_f32_16x16x32_bf16 v[124:127], v[148:151], v[188:191], 0
	v_mfma_f32_16x16x32_bf16 v[116:119], v[156:159], v[188:191], 0
	v_mfma_f32_16x16x32_bf16 v[108:111], v[148:151], v[196:199], 0
	v_mfma_f32_16x16x32_bf16 v[100:103], v[156:159], v[196:199], 0
	v_mfma_f32_16x16x32_bf16 v[92:95], v[148:151], v[204:207], 0
	v_mfma_f32_16x16x32_bf16 v[84:87], v[156:159], v[204:207], 0
	v_mfma_f32_16x16x32_bf16 v[76:79], v[148:151], v[212:215], 0
	v_mfma_f32_16x16x32_bf16 v[68:71], v[156:159], v[212:215], 0
	v_mfma_f32_16x16x32_bf16 v[124:127], v[152:155], v[192:195], v[124:127]
	v_mfma_f32_16x16x32_bf16 v[116:119], v[160:163], v[192:195], v[116:119]
	v_mfma_f32_16x16x32_bf16 v[108:111], v[152:155], v[200:203], v[108:111]
	v_mfma_f32_16x16x32_bf16 v[100:103], v[160:163], v[200:203], v[100:103]
	v_mfma_f32_16x16x32_bf16 v[92:95], v[152:155], v[208:211], v[92:95]
	v_mfma_f32_16x16x32_bf16 v[84:87], v[160:163], v[208:211], v[84:87]
	v_mfma_f32_16x16x32_bf16 v[76:79], v[152:155], v[216:219], v[76:79]
	v_mfma_f32_16x16x32_bf16 v[68:71], v[160:163], v[216:219], v[68:71]
	s_setprio 0
	s_setprio 1
	v_mfma_f32_16x16x32_bf16 v[120:123], v[172:175], v[188:191], 0
	v_mfma_f32_16x16x32_bf16 v[112:115], v[180:183], v[188:191], 0
	v_mfma_f32_16x16x32_bf16 v[104:107], v[172:175], v[196:199], 0
	v_mfma_f32_16x16x32_bf16 v[96:99], v[180:183], v[196:199], 0
	v_mfma_f32_16x16x32_bf16 v[88:91], v[172:175], v[204:207], 0
	v_mfma_f32_16x16x32_bf16 v[80:83], v[180:183], v[204:207], 0
	v_mfma_f32_16x16x32_bf16 v[72:75], v[172:175], v[212:215], 0
	v_mfma_f32_16x16x32_bf16 v[64:67], v[180:183], v[212:215], 0
	v_mfma_f32_16x16x32_bf16 v[120:123], v[176:179], v[192:195], v[120:123]
	v_mfma_f32_16x16x32_bf16 v[112:115], v[184:187], v[192:195], v[112:115]
	v_mfma_f32_16x16x32_bf16 v[104:107], v[176:179], v[200:203], v[104:107]
	v_mfma_f32_16x16x32_bf16 v[96:99], v[184:187], v[200:203], v[96:99]
	v_mfma_f32_16x16x32_bf16 v[88:91], v[176:179], v[208:211], v[88:91]
	v_mfma_f32_16x16x32_bf16 v[80:83], v[184:187], v[208:211], v[80:83]
	v_mfma_f32_16x16x32_bf16 v[72:75], v[176:179], v[216:219], v[72:75]
	v_mfma_f32_16x16x32_bf16 v[64:67], v[184:187], v[216:219], v[64:67]
	s_setprio 0
	s_barrier
	s_add_i32 s68, s45, s33
	s_add_u32 s98, s26, 0x80
	s_addc_u32 s99, s27, 0
	s_mov_b32 m0, s68
	ds_read_b128 v[188:191], v168 offset:16384
	ds_read_b128 v[192:195], v168 offset:17408
	ds_read_b128 v[196:199], v168 offset:18432
	ds_read_b128 v[200:203], v168 offset:19456
	ds_read_b128 v[204:207], v168 offset:20480
	ds_read_b128 v[208:211], v168 offset:21504
	ds_read_b128 v[212:215], v168 offset:22528
	ds_read_b128 v[216:219], v168 offset:23552
	global_load_lds_dwordx4 v132, s[26:27]
	s_add_i32 m0, s68, 0x2000
	s_add_u32 s68, s26, 0x40000
	s_addc_u32 s69, s27, 0
	s_add_i32 s70, s46, s33
	global_load_lds_dwordx4 v128, s[26:27]
	s_mov_b32 m0, s70
	s_add_u32 s100, s28, 0x80
	s_addc_u32 s101, s29, 0
	global_load_lds_dwordx4 v132, s[68:69]
	s_add_i32 m0, s70, 0x2000
	s_nop 0
	global_load_lds_dwordx4 v128, s[68:69]
	s_mov_b32 m0, s36
	s_nop 0
	global_load_lds_dwordx4 v134, s[28:29]
	s_mov_b32 m0, s37
	s_nop 0
	global_load_lds_dwordx4 v130, s[28:29]
	s_waitcnt vmcnt(8) lgkmcnt(0)
	s_barrier
; #define PG8_STAGE(bufoff, gbase, voff) do { _Pragma("unroll") for (int _i = 0; _i < 2; ++_i) \
;         __builtin_amdgcn_global_load_lds((const unsigned*)((const char*)(gbase) + (voff)[_i]), (PG8_LAS unsigned*)(lds + (bufoff) + ldsw + _i * 8192), 16, 0, 0); } while (0)
; #define PG8_LDA(dst, b, h) do { _Pragma("unroll") for (int m = 0; m < 4; ++m) _Pragma("unroll") for (int k = 0; k < 2; ++k) dst[m][k] = *(const PG8_LAS bf16x8*)(lds + PG8_SA(b, h) + aoff + m * 2048 + k * 1024); } while (0)
; #define PG8_LDB(dst, b, h) do { _Pragma("unroll") for (int n = 0; n < 2; ++n) _Pragma("unroll") for (int k = 0; k < 2; ++k) dst[n][k] = *(const PG8_LAS bf16x8*)(lds + PG8_SB(b, h) + boff + n * 2048 + k * 1024); } while (0)
; #define PG8_MMA(ai, bj, At, Bt) do { __builtin_amdgcn_s_setprio(1); _Pragma("unroll") for (int m = 0; m < 4; ++m) _Pragma("unroll") for (int n = 0; n < 2; ++n) _Pragma("unroll") for (int k = 0; k < 2; ++k) \
;         acc[ai][bj][m][n] = __builtin_amdgcn_mfma_f32_16x16x32_bf16(Bt[n][k], At[m][k], acc[ai][bj][m][n], 0, 0, 0); __builtin_amdgcn_s_setprio(0); } while (0)
; #define PG8_WAIT_V(n) asm volatile("s_waitcnt vmcnt(" #n ")" ::: "memory")
; #define PG8_WAIT_L(n) asm volatile("s_waitcnt lgkmcnt(" #n ")" ::: "memory")
; #define PG8_BAR __builtin_amdgcn_s_barrier()
; #define PG8_SCHED __builtin_amdgcn_sched_barrier(0)
; template <class Epi, class Sched, bool ALIGN_EPI = false, bool SP2 = false>
; __device__ __forceinline__ void gemm_phase(PG8_LAS unsigned char* lds, const Gemm g, const Sched& S, const Epi& E, const int wid) {
;     ...
;             PG8_LDB(B0, 0, 0); PG8_LDB(B1, 0, 1); PG8_SCHED; PG8_LDA(At, 0, 0); PG8_STAGE(PG8_SA(1, 1), a1 + hstepA, voffA);
;             PG8_WAIT_V(8); PG8_WAIT_L(0); PG8_BAR; PG8_MMA(0, 0, At, B0); PG8_MMA(0, 1, At, B1); PG8_BAR; PG8_SCHED;
;             PG8_LDA(At, 0, 1); PG8_STAGE(PG8_SB(0, 0), b2, voffB); PG8_STAGE(PG8_SB(0, 1), b2 + hstepB, voffB); PG8_STAGE(PG8_SA(0, 0), a2, voffA);
;             PG8_WAIT_V(8); PG8_WAIT_L(0); PG8_BAR; PG8_MMA(1, 0, At, B0); PG8_MMA(1, 1, At, B1); PG8_BAR; PG8_SCHED;
;             PG8_LDB(B0, 1, 0); PG8_LDB(B1, 1, 1); PG8_SCHED; PG8_LDA(At, 1, 0); PG8_STAGE(PG8_SA(0, 1), a2 + hstepA, voffA);
;             PG8_WAIT_V(8); PG8_WAIT_L(0); PG8_BAR; PG8_MMA(0, 0, At, B0); PG8_MMA(0, 1, At, B1); PG8_BAR; PG8_SCHED;
	s_setprio 1
	v_mfma_f32_16x16x32_bf16 v[60:63], v[148:151], v[188:191], 0
	v_mfma_f32_16x16x32_bf16 v[52:55], v[156:159], v[188:191], 0
	v_mfma_f32_16x16x32_bf16 v[44:47], v[148:151], v[196:199], 0
	v_mfma_f32_16x16x32_bf16 v[36:39], v[156:159], v[196:199], 0
	v_mfma_f32_16x16x32_bf16 v[28:31], v[148:151], v[204:207], 0
	v_mfma_f32_16x16x32_bf16 v[20:23], v[156:159], v[204:207], 0
	v_mfma_f32_16x16x32_bf16 v[12:15], v[148:151], v[212:215], 0
	v_mfma_f32_16x16x32_bf16 v[4:7], v[156:159], v[212:215], 0
	v_mfma_f32_16x16x32_bf16 v[60:63], v[152:155], v[192:195], v[60:63]
	v_mfma_f32_16x16x32_bf16 v[52:55], v[160:163], v[192:195], v[52:55]
	v_mfma_f32_16x16x32_bf16 v[44:47], v[152:155], v[200:203], v[44:47]
	v_mfma_f32_16x16x32_bf16 v[36:39], v[160:163], v[200:203], v[36:39]
	v_mfma_f32_16x16x32_bf16 v[28:31], v[152:155], v[208:211], v[28:31]
	v_mfma_f32_16x16x32_bf16 v[20:23], v[160:163], v[208:211], v[20:23]
	v_mfma_f32_16x16x32_bf16 v[12:15], v[152:155], v[216:219], v[12:15]
	v_mfma_f32_16x16x32_bf16 v[4:7], v[160:163], v[216:219], v[4:7]
	s_setprio 0
	s_setprio 1
	v_mfma_f32_16x16x32_bf16 v[56:59], v[172:175], v[188:191], 0
	v_mfma_f32_16x16x32_bf16 v[48:51], v[180:183], v[188:191], 0
	v_mfma_f32_16x16x32_bf16 v[40:43], v[172:175], v[196:199], 0
	v_mfma_f32_16x16x32_bf16 v[32:35], v[180:183], v[196:199], 0
	v_mfma_f32_16x16x32_bf16 v[24:27], v[172:175], v[204:207], 0
	v_mfma_f32_16x16x32_bf16 v[16:19], v[180:183], v[204:207], 0
	v_mfma_f32_16x16x32_bf16 v[8:11], v[172:175], v[212:215], 0
	v_mfma_f32_16x16x32_bf16 v[0:3], v[180:183], v[212:215], 0
	v_mfma_f32_16x16x32_bf16 v[56:59], v[176:179], v[192:195], v[56:59]
	v_mfma_f32_16x16x32_bf16 v[48:51], v[184:187], v[192:195], v[48:51]
	v_mfma_f32_16x16x32_bf16 v[40:43], v[176:179], v[200:203], v[40:43]
	v_mfma_f32_16x16x32_bf16 v[32:35], v[184:187], v[200:203], v[32:35]
	v_mfma_f32_16x16x32_bf16 v[24:27], v[176:179], v[208:211], v[24:27]
	v_mfma_f32_16x16x32_bf16 v[16:19], v[184:187], v[208:211], v[16:19]
	v_mfma_f32_16x16x32_bf16 v[8:11], v[176:179], v[216:219], v[8:11]
	v_mfma_f32_16x16x32_bf16 v[0:3], v[184:187], v[216:219], v[0:3]
	s_setprio 0
	s_barrier
	s_add_i32 s68, 0, 0x18000
	s_add_i32 s69, 0, 0x1c000
	ds_read_b128 v[148:151], v252
	ds_read_b128 v[152:155], v252 offset:1024
	ds_read_b128 v[156:159], v252 offset:2048
	ds_read_b128 v[160:163], v252 offset:3072
	ds_read_b128 v[172:175], v253
	ds_read_b128 v[176:179], v253 offset:1024
	ds_read_b128 v[180:183], v253 offset:2048
	ds_read_b128 v[184:187], v253 offset:3072
	s_add_u32 s28, s28, 0x40000
	s_addc_u32 s29, s29, 0
	s_mov_b32 m0, s38
	ds_read_b128 v[188:191], v168 offset:32768
	ds_read_b128 v[192:195], v168 offset:33792
	ds_read_b128 v[196:199], v168 offset:34816
	ds_read_b128 v[200:203], v168 offset:35840
	ds_read_b128 v[204:207], v168 offset:36864
	ds_read_b128 v[208:211], v168 offset:37888
	ds_read_b128 v[212:215], v168 offset:38912
	ds_read_b128 v[216:219], v168 offset:39936
	global_load_lds_dwordx4 v134, s[28:29]
	s_mov_b32 m0, s39
	s_nop 0
	global_load_lds_dwordx4 v130, s[28:29]
	s_waitcnt vmcnt(8) lgkmcnt(0)
	s_barrier
	s_setprio 1
	v_mfma_f32_16x16x32_bf16 v[124:127], v[148:151], v[188:191], v[124:127]
	v_mfma_f32_16x16x32_bf16 v[116:119], v[156:159], v[188:191], v[116:119]
	v_mfma_f32_16x16x32_bf16 v[108:111], v[148:151], v[196:199], v[108:111]
	v_mfma_f32_16x16x32_bf16 v[100:103], v[156:159], v[196:199], v[100:103]
	v_mfma_f32_16x16x32_bf16 v[92:95], v[148:151], v[204:207], v[92:95]
	v_mfma_f32_16x16x32_bf16 v[84:87], v[156:159], v[204:207], v[84:87]
	v_mfma_f32_16x16x32_bf16 v[76:79], v[148:151], v[212:215], v[76:79]
	v_mfma_f32_16x16x32_bf16 v[68:71], v[156:159], v[212:215], v[68:71]
	v_mfma_f32_16x16x32_bf16 v[124:127], v[152:155], v[192:195], v[124:127]
	v_mfma_f32_16x16x32_bf16 v[116:119], v[160:163], v[192:195], v[116:119]
	v_mfma_f32_16x16x32_bf16 v[108:111], v[152:155], v[200:203], v[108:111]
	v_mfma_f32_16x16x32_bf16 v[100:103], v[160:163], v[200:203], v[100:103]
	v_mfma_f32_16x16x32_bf16 v[92:95], v[152:155], v[208:211], v[92:95]
	v_mfma_f32_16x16x32_bf16 v[84:87], v[160:163], v[208:211], v[84:87]
	v_mfma_f32_16x16x32_bf16 v[76:79], v[152:155], v[216:219], v[76:79]
	v_mfma_f32_16x16x32_bf16 v[68:71], v[160:163], v[216:219], v[68:71]
	s_setprio 0
	s_setprio 1
	v_mfma_f32_16x16x32_bf16 v[120:123], v[172:175], v[188:191], v[120:123]
	v_mfma_f32_16x16x32_bf16 v[112:115], v[180:183], v[188:191], v[112:115]
	v_mfma_f32_16x16x32_bf16 v[104:107], v[172:175], v[196:199], v[104:107]
	v_mfma_f32_16x16x32_bf16 v[96:99], v[180:183], v[196:199], v[96:99]
	v_mfma_f32_16x16x32_bf16 v[88:91], v[172:175], v[204:207], v[88:91]
	v_mfma_f32_16x16x32_bf16 v[80:83], v[180:183], v[204:207], v[80:83]
	v_mfma_f32_16x16x32_bf16 v[72:75], v[172:175], v[212:215], v[72:75]
	v_mfma_f32_16x16x32_bf16 v[64:67], v[180:183], v[212:215], v[64:67]
	v_mfma_f32_16x16x32_bf16 v[120:123], v[176:179], v[192:195], v[120:123]
	v_mfma_f32_16x16x32_bf16 v[112:115], v[184:187], v[192:195], v[112:115]
	v_mfma_f32_16x16x32_bf16 v[104:107], v[176:179], v[200:203], v[104:107]
	v_mfma_f32_16x16x32_bf16 v[96:99], v[184:187], v[200:203], v[96:99]
	v_mfma_f32_16x16x32_bf16 v[88:91], v[176:179], v[208:211], v[88:91]
	v_mfma_f32_16x16x32_bf16 v[80:83], v[184:187], v[208:211], v[80:83]
	v_mfma_f32_16x16x32_bf16 v[72:75], v[176:179], v[216:219], v[72:75]
	v_mfma_f32_16x16x32_bf16 v[64:67], v[184:187], v[216:219], v[64:67]
	s_setprio 0
	s_barrier
; #define PG8_STAGE(bufoff, gbase, voff) do { _Pragma("unroll") for (int _i = 0; _i < 2; ++_i) \
;         __builtin_amdgcn_global_load_lds((const unsigned*)((const char*)(gbase) + (voff)[_i]), (PG8_LAS unsigned*)(lds + (bufoff) + ldsw + _i * 8192), 16, 0, 0); } while (0)
; #define PG8_LDA(dst, b, h) do { _Pragma("unroll") for (int m = 0; m < 4; ++m) _Pragma("unroll") for (int k = 0; k < 2; ++k) dst[m][k] = *(const PG8_LAS bf16x8*)(lds + PG8_SA(b, h) + aoff + m * 2048 + k * 1024); } while (0)
; #define PG8_MMA(ai, bj, At, Bt) do { __builtin_amdgcn_s_setprio(1); _Pragma("unroll") for (int m = 0; m < 4; ++m) _Pragma("unroll") for (int n = 0; n < 2; ++n) _Pragma("unroll") for (int k = 0; k < 2; ++k) \
;         acc[ai][bj][m][n] = __builtin_amdgcn_mfma_f32_16x16x32_bf16(Bt[n][k], At[m][k], acc[ai][bj][m][n], 0, 0, 0); __builtin_amdgcn_s_setprio(0); } while (0)
; #define PG8_WAIT_V(n) asm volatile("s_waitcnt vmcnt(" #n ")" ::: "memory")
; #define PG8_WAIT_L(n) asm volatile("s_waitcnt lgkmcnt(" #n ")" ::: "memory")
; #define PG8_BAR __builtin_amdgcn_s_barrier()
; #define PG8_SCHED __builtin_amdgcn_sched_barrier(0)
; template <class Epi, class Sched, bool ALIGN_EPI = false, bool SP2 = false>
; __device__ __forceinline__ void gemm_phase(PG8_LAS unsigned char* lds, const Gemm g, const Sched& S, const Epi& E, const int wid) {
;     ...
;         for (int t = 0; t < nt; t += 2) {
;             const bool last = (t == nt - 2);
;             const char* a1 = cA + (size_t)(t + 1) * kstep;
;             const char* a2 = last ? nA : cA + (size_t)(t + 2) * kstep; const char* b2 = last ? nB : cB + (size_t)(t + 2) * kstep;
;             const char* a3 = a2 + kstep; const char* b3 = b2 + kstep;
;             if (last && has_next) S.a_ready(nxt);
;     ...
;             PG8_LDA(At, 1, 1); PG8_STAGE(PG8_SB(1, 0), b3, voffB); PG8_STAGE(PG8_SB(1, 1), b3 + hstepB, voffB); PG8_STAGE(PG8_SA(1, 0), a3, voffA);
;             PG8_WAIT_V(8); PG8_WAIT_L(0); PG8_BAR; PG8_MMA(1, 0, At, B0); PG8_MMA(1, 1, At, B1); PG8_BAR; PG8_SCHED;
	s_add_i32 s28, s68, s33
	s_mov_b32 m0, s28
	ds_read_b128 v[188:191], v168 offset:49152
	ds_read_b128 v[192:195], v168 offset:50176
	ds_read_b128 v[196:199], v168 offset:51200
	ds_read_b128 v[200:203], v168 offset:52224
	ds_read_b128 v[204:207], v168 offset:53248
	ds_read_b128 v[208:211], v168 offset:54272
	ds_read_b128 v[212:215], v168 offset:55296
	ds_read_b128 v[216:219], v168 offset:56320
	global_load_lds_dwordx4 v132, s[98:99]
	s_add_i32 m0, s28, 0x2000
	s_add_u32 s26, s26, 0x40080
	s_addc_u32 s27, s27, 0
	s_add_i32 s28, s69, s33
	global_load_lds_dwordx4 v128, s[98:99]
	s_mov_b32 m0, s28
	s_nop 0
	global_load_lds_dwordx4 v132, s[26:27]
	s_add_i32 m0, s28, 0x2000
	s_nop 0
	global_load_lds_dwordx4 v128, s[26:27]
	s_mov_b32 m0, s40
	s_nop 0
	global_load_lds_dwordx4 v134, s[100:101]
	s_mov_b32 m0, s41
	s_nop 0
	global_load_lds_dwordx4 v130, s[100:101]
	s_waitcnt vmcnt(8) lgkmcnt(0)
	s_barrier
	s_setprio 1
	v_mfma_f32_16x16x32_bf16 v[60:63], v[148:151], v[188:191], v[60:63]
	v_mfma_f32_16x16x32_bf16 v[52:55], v[156:159], v[188:191], v[52:55]
	v_mfma_f32_16x16x32_bf16 v[44:47], v[148:151], v[196:199], v[44:47]
	v_mfma_f32_16x16x32_bf16 v[36:39], v[156:159], v[196:199], v[36:39]
	v_mfma_f32_16x16x32_bf16 v[28:31], v[148:151], v[204:207], v[28:31]
	v_mfma_f32_16x16x32_bf16 v[20:23], v[156:159], v[204:207], v[20:23]
	v_mfma_f32_16x16x32_bf16 v[12:15], v[148:151], v[212:215], v[12:15]
	v_mfma_f32_16x16x32_bf16 v[4:7], v[156:159], v[212:215], v[4:7]
	v_mfma_f32_16x16x32_bf16 v[60:63], v[152:155], v[192:195], v[60:63]
	v_mfma_f32_16x16x32_bf16 v[52:55], v[160:163], v[192:195], v[52:55]
	v_mfma_f32_16x16x32_bf16 v[44:47], v[152:155], v[200:203], v[44:47]
	v_mfma_f32_16x16x32_bf16 v[36:39], v[160:163], v[200:203], v[36:39]
	v_mfma_f32_16x16x32_bf16 v[28:31], v[152:155], v[208:211], v[28:31]
	v_mfma_f32_16x16x32_bf16 v[20:23], v[160:163], v[208:211], v[20:23]
	v_mfma_f32_16x16x32_bf16 v[12:15], v[152:155], v[216:219], v[12:15]
	v_mfma_f32_16x16x32_bf16 v[4:7], v[160:163], v[216:219], v[4:7]
	s_setprio 0
	s_setprio 1
	v_mfma_f32_16x16x32_bf16 v[56:59], v[172:175], v[188:191], v[56:59]
	v_mfma_f32_16x16x32_bf16 v[48:51], v[180:183], v[188:191], v[48:51]
	v_mfma_f32_16x16x32_bf16 v[40:43], v[172:175], v[196:199], v[40:43]
	v_mfma_f32_16x16x32_bf16 v[32:35], v[180:183], v[196:199], v[32:35]
	v_mfma_f32_16x16x32_bf16 v[24:27], v[172:175], v[204:207], v[24:27]
	v_mfma_f32_16x16x32_bf16 v[16:19], v[180:183], v[204:207], v[16:19]
	v_mfma_f32_16x16x32_bf16 v[8:11], v[172:175], v[212:215], v[8:11]
	v_mfma_f32_16x16x32_bf16 v[0:3], v[180:183], v[212:215], v[0:3]
	v_mfma_f32_16x16x32_bf16 v[56:59], v[176:179], v[192:195], v[56:59]
	v_mfma_f32_16x16x32_bf16 v[48:51], v[184:187], v[192:195], v[48:51]
	v_mfma_f32_16x16x32_bf16 v[40:43], v[176:179], v[200:203], v[40:43]
	v_mfma_f32_16x16x32_bf16 v[32:35], v[184:187], v[200:203], v[32:35]
	v_mfma_f32_16x16x32_bf16 v[24:27], v[176:179], v[208:211], v[24:27]
	v_mfma_f32_16x16x32_bf16 v[16:19], v[184:187], v[208:211], v[16:19]
	v_mfma_f32_16x16x32_bf16 v[8:11], v[176:179], v[216:219], v[8:11]
	v_mfma_f32_16x16x32_bf16 v[0:3], v[184:187], v[216:219], v[0:3]
	s_setprio 0
	s_barrier
	s_add_i32 s67, s67, 2
	s_add_u32 s24, s24, 0x100
	s_addc_u32 s25, s25, 0
	s_add_u32 s65, s65, 0x100
	s_addc_u32 s66, s66, 0
	s_cmp_gt_u32 s67, 13

;     __device__ __forceinline__ void operator()(const f32x4 (&acc)[2][2][4][2], const Unit& u, int wr, int wc, int fr, int fq) const {
;         float xv[2][4];
;         {
;             f32x4 qd[2][4];
; #pragma unroll
;             for (int ai = 0; ai < 2; ++ai)
; #pragma unroll
;                 for (int m = 0; m < 4; ++m) qd[ai][m] = row_quad(ssq, u.pm * BM + ai * HALF + wr * 64 + m * 16 + fr, fq);
; #pragma unroll
;             for (int ai = 0; ai < 2; ++ai)
; #pragma unroll
;                 for (int m = 0; m < 4; ++m) asm volatile("" : "+v"(qd[ai][m]));
; #pragma unroll
;             for (int ai = 0; ai < 2; ++ai)
; #pragma unroll
;                 for (int m = 0; m < 4; ++m) xv[ai][m] = row_ms_from_quad(qd[ai][m], 1.0f / 1024.0f);
;         }
; #pragma unroll
;         for (int ai = 0; ai < 2; ++ai)
; #pragma unroll
;             for (int m = 0; m < 4; ++m) {
;                 const int row = u.pm * BM + ai * HALF + wr * 64 + m * 16 + fr;
;                 const float x = xv[ai][m], rs = __builtin_amdgcn_rsqf(x);
.LBB0_1870:
	v_lshl_add_u32 v162, s22, 8, v164
	v_or_b32_e32 v160, 16, v162
	v_or_b32_e32 v158, 32, v162
	v_or_b32_e32 v156, 48, v162
	v_add_u32_e32 v154, 0x80, v162
	v_add_u32_e32 v152, 0x90, v162
	v_add_u32_e32 v150, 0xa0, v162
	v_add_u32_e32 v148, 0xb0, v162
	v_and_b32_e32 v151, 64, v169
	v_xor_b32_e32 v149, 16, v169
	v_add_u32_e32 v151, 64, v151
	v_xor_b32_e32 v153, 32, v169
	v_cmp_lt_i32_e32 vcc, v149, v151
	v_mul_f32_e32 v120, v124, v120
	v_mul_f32_e32 v121, v125, v121
	v_cndmask_b32_e32 v149, v169, v149, vcc
	v_cmp_lt_i32_e32 vcc, v153, v151
	v_lshlrev_b32_e32 v149, 2, v149
	v_mul_f32_e32 v122, v126, v122
	v_cndmask_b32_e32 v151, v169, v153, vcc
	v_lshlrev_b32_e32 v151, 2, v151
	v_mul_f32_e32 v112, v116, v112
	v_mul_f32_e32 v113, v117, v113
	v_mul_f32_e32 v114, v118, v114
	s_lshl_b32 s22, s23, 7
	v_mul_f32_e32 v123, v127, v123
	s_ashr_i32 s23, s22, 31
	s_lshl_b64 s[22:23], s[22:23], 1
	v_mul_f32_e32 v104, v108, v104
	v_mul_f32_e32 v105, v109, v105
	v_mul_f32_e32 v106, v110, v106
	v_mul_f32_e32 v96, v100, v96
	v_mul_f32_e32 v97, v101, v97
	v_mul_f32_e32 v107, v111, v107
	v_mul_f32_e32 v98, v102, v98
	v_mul_f32_e32 v88, v92, v88
	v_mul_f32_e32 v89, v93, v89
	v_mul_f32_e32 v90, v94, v90
	v_mul_f32_e32 v80, v84, v80
	v_mul_f32_e32 v81, v85, v81
	v_mul_f32_e32 v91, v95, v91
	v_mul_f32_e32 v82, v86, v82
	v_mul_f32_e32 v72, v76, v72
	v_mul_f32_e32 v73, v77, v73
	v_mul_f32_e32 v74, v78, v74
	v_mul_f32_e32 v64, v68, v64
	v_mul_f32_e32 v65, v69, v65
	v_mul_f32_e32 v75, v79, v75
	v_mul_f32_e32 v66, v70, v66
	v_mul_f32_e32 v56, v60, v56
	v_mul_f32_e32 v57, v61, v57
	v_mul_f32_e32 v58, v62, v58
	v_mul_f32_e32 v48, v52, v48
	v_mul_f32_e32 v49, v53, v49
	v_mul_f32_e32 v59, v63, v59
	v_mul_f32_e32 v50, v54, v50
	v_mul_f32_e32 v40, v44, v40
	v_mul_f32_e32 v41, v45, v41
	v_mul_f32_e32 v42, v46, v42
	v_mul_f32_e32 v32, v36, v32
	v_mul_f32_e32 v33, v37, v33
	s_nop 0
	v_add_f32_e32 v153, v220, v221
	v_add_f32_e32 v153, v222, v153
	v_add_f32_e32 v155, v224, v225
	v_add_f32_e32 v153, v223, v153
	v_add_f32_e32 v155, v226, v155
	ds_bpermute_b32 v171, v149, v153
	v_add_f32_e32 v155, v227, v155
	ds_bpermute_b32 v172, v149, v155
	v_add_f32_e32 v157, v228, v229
	v_add_f32_e32 v157, v230, v157
	v_add_f32_e32 v159, v232, v233
	v_add_f32_e32 v159, v234, v159
	v_add_f32_e32 v157, v231, v157
	v_add_f32_e32 v159, v235, v159
	ds_bpermute_b32 v173, v149, v157
	ds_bpermute_b32 v174, v149, v159
	s_waitcnt lgkmcnt(3)
	v_add_f32_e32 v153, v153, v171
	ds_bpermute_b32 v171, v151, v153
	v_add_f32_e32 v161, v236, v237
	s_waitcnt lgkmcnt(3)
	v_add_f32_e32 v155, v155, v172
	v_add_f32_e32 v161, v238, v161
	ds_bpermute_b32 v172, v151, v155
	v_add_f32_e32 v161, v239, v161
	ds_bpermute_b32 v175, v149, v161
	s_waitcnt lgkmcnt(4)
	v_add_f32_e32 v157, v157, v173
	s_waitcnt lgkmcnt(3)
	v_add_f32_e32 v159, v159, v174
	ds_bpermute_b32 v173, v151, v157
	ds_bpermute_b32 v174, v151, v159
	v_add_f32_e32 v163, v240, v241
	s_waitcnt lgkmcnt(4)
	v_add_f32_e32 v153, v153, v171
	v_add_f32_e32 v163, v242, v163
	v_fmamk_f32 v171, v153, 0x3a800000, v170
	s_waitcnt lgkmcnt(3)
	v_add_f32_e32 v153, v155, v172
	v_add_f32_e32 v172, v244, v245
	v_add_f32_e32 v163, v243, v163
	v_add_f32_e32 v172, v246, v172
	ds_bpermute_b32 v176, v149, v163
	s_waitcnt lgkmcnt(3)
	v_add_f32_e32 v161, v161, v175
	v_add_f32_e32 v172, v247, v172
	ds_bpermute_b32 v175, v151, v161
	s_waitcnt lgkmcnt(3)
	v_add_f32_e32 v155, v157, v173
	ds_bpermute_b32 v173, v149, v172
	s_waitcnt lgkmcnt(3)
	v_add_f32_e32 v157, v159, v174
	v_add_f32_e32 v174, v248, v249
	v_add_f32_e32 v174, v250, v174
	v_add_f32_e32 v174, v251, v174
	s_waitcnt lgkmcnt(2)
	v_add_f32_e32 v163, v163, v176
	ds_bpermute_b32 v149, v149, v174
	s_waitcnt lgkmcnt(2)
	v_add_f32_e32 v159, v161, v175
	v_fmamk_f32 v161, v153, 0x3a800000, v170
	ds_bpermute_b32 v153, v151, v163
	s_waitcnt lgkmcnt(2)
	v_add_f32_e32 v172, v172, v173
	ds_bpermute_b32 v173, v151, v172
	s_waitcnt lgkmcnt(2)
	v_add_f32_e32 v149, v174, v149
	v_fmamk_f32 v155, v155, 0x3a800000, v170
	s_waitcnt lgkmcnt(1)
	v_add_f32_e32 v153, v163, v153
	ds_bpermute_b32 v163, v151, v149
	s_waitcnt lgkmcnt(1)
	v_add_f32_e32 v151, v172, v173
	v_rsq_f32_e32 v172, v171
	v_fmamk_f32 v157, v157, 0x3a800000, v170
	v_fmamk_f32 v159, v159, 0x3a800000, v170
	s_waitcnt lgkmcnt(0)
; __device__ __forceinline__ unsigned cvt_pk_bf16(float lo, float hi) { unsigned r; asm volatile("v_cvt_pk_bf16_f32 %0, %1, %2" : "=v"(r) : "v"(lo), "v"(hi)); return r; }
;     __device__ __forceinline__ void operator()(const f32x4 (&acc)[2][2][4][2], const Unit& u, int wr, int wc, int fr, int fq) const {
;     ...
;             for (int m = 0; m < 4; ++m) {
;                 const int row = u.pm * BM + ai * HALF + wr * 64 + m * 16 + fr;
;                 const float x = xv[ai][m], rs = __builtin_amdgcn_rsqf(x);
;                 const float ea = -1.4426950408889634f * rs;
;                 float h[8];
; #pragma unroll
;                 for (int n = 0; n < 2; ++n)
; #pragma unroll
;                     for (int j = 0; j < 4; ++j) {
;                         const float g = acc[ai][0][m][n][j], uu = acc[ai][1][m][n][j];
;                         const float e = __builtin_amdgcn_exp2f(g * ea);
;                         const float q = __builtin_amdgcn_rcpf(__builtin_fmaf(e, x, x));
;                         h[n * 4 + j] = (g * uu) * q;
;                     }
;                 u32x4 w; w.x = cvt_pk_bf16(h[0], h[1]); w.y = cvt_pk_bf16(h[2], h[3]); w.z = cvt_pk_bf16(h[4], h[5]); w.w = cvt_pk_bf16(h[6], h[7]);
;                 *(u32x4*)(Hd + (size_t)row * ldh + u.pn * HALF + wc * 32 + 8 * fq) = w;
	v_add_f32_e32 v149, v149, v163
	v_mul_f32_e32 v163, 0xbfb8aa3b, v172
	v_mul_f32_e32 v173, v125, v163
	v_exp_f32_e32 v173, v173
	v_mul_f32_e32 v172, v124, v163
	v_exp_f32_e32 v172, v172
	v_mul_f32_e32 v125, v127, v163
	v_fma_f32 v124, v173, v171, v171
	v_mul_f32_e32 v173, v126, v163
	v_rcp_f32_e32 v124, v124
	v_exp_f32_e32 v173, v173
	v_mul_f32_e32 v126, v117, v163
	v_exp_f32_e32 v126, v126
	v_mul_f32_e32 v121, v121, v124
	v_fma_f32 v124, v173, v171, v171
	v_rcp_f32_e32 v124, v124
	v_mul_f32_e32 v117, v118, v163
	v_exp_f32_e32 v117, v117
	v_exp_f32_e32 v125, v125
	v_mul_f32_e32 v122, v122, v124
	v_mul_f32_e32 v124, v116, v163
	v_exp_f32_e32 v124, v124
	v_fma_f32 v116, v126, v171, v171
	v_rcp_f32_e32 v116, v116
	v_fma_f32 v172, v172, v171, v171
	v_fma_f32 v124, v124, v171, v171
	v_rcp_f32_e32 v124, v124
	v_mul_f32_e32 v113, v113, v116
	v_fma_f32 v116, v117, v171, v171
	v_rcp_f32_e32 v172, v172
	v_mul_f32_e32 v112, v112, v124
	v_mul_f32_e32 v124, v119, v163
	v_exp_f32_e32 v124, v124
	v_fma_f32 v125, v125, v171, v171
	v_rcp_f32_e32 v116, v116
	v_rcp_f32_e32 v125, v125
	v_fmac_f32_e32 v171, v124, v171
	v_rcp_f32_e32 v117, v171
	v_mul_f32_e32 v120, v120, v172
	v_mul_f32_e32 v118, v114, v116
	v_mul_f32_e32 v114, v119, v115
	v_mul_f32_e32 v123, v123, v125
	v_mul_f32_e32 v117, v114, v117
	v_cvt_pk_bf16_f32 v114, v120, v121
	v_cvt_pk_bf16_f32 v115, v122, v123
	v_cvt_pk_bf16_f32 v116, v112, v113
	v_mov_b64_e32 v[112:113], s[8:9]
	v_rsq_f32_e32 v120, v161
	v_cvt_pk_bf16_f32 v117, v118, v117
	v_mad_i64_i32 v[118:119], s[24:25], v162, s47, v[112:113]
	v_lshl_add_u64 v[118:119], v[118:119], 0, s[22:23]
	v_lshl_add_u64 v[118:119], v[118:119], 0, s[4:5]
	v_lshl_add_u64 v[118:119], v[118:119], 0, v[136:137]
	v_mul_f32_e32 v120, 0xbfb8aa3b, v120
	global_store_dwordx4 v[118:119], v[114:117], off
	v_mul_f32_e32 v121, v108, v120
	v_exp_f32_e32 v121, v121
	v_mul_f32_e32 v114, v109, v120
	v_exp_f32_e32 v114, v114
	v_mul_f32_e32 v109, v111, v120
	v_exp_f32_e32 v109, v109
	v_fma_f32 v115, v121, v161, v161
	v_fma_f32 v108, v114, v161, v161
	v_mul_f32_e32 v114, v110, v120
	v_rcp_f32_e32 v108, v108
	v_exp_f32_e32 v114, v114
	v_mul_f32_e32 v110, v101, v120
	v_exp_f32_e32 v110, v110
	v_mul_f32_e32 v105, v105, v108
	v_fma_f32 v108, v114, v161, v161
	v_rcp_f32_e32 v108, v108
	v_fma_f32 v109, v109, v161, v161
	v_mul_f32_e32 v101, v102, v120
	v_rcp_f32_e32 v109, v109
	v_mul_f32_e32 v106, v106, v108
	v_mul_f32_e32 v108, v100, v120
	v_exp_f32_e32 v108, v108
	v_exp_f32_e32 v101, v101
	v_mul_f32_e32 v107, v107, v109
	v_rcp_f32_e32 v115, v115
	v_fma_f32 v108, v108, v161, v161
	v_rcp_f32_e32 v108, v108
	v_rsq_f32_e32 v102, v155
	v_mul_f32_e32 v104, v104, v115
	v_fmamk_f32 v153, v153, 0x3a800000, v170
	v_mul_f32_e32 v100, v96, v108
	v_fma_f32 v96, v110, v161, v161
	v_rcp_f32_e32 v96, v96
	v_mul_f32_e32 v108, v103, v120
	v_exp_f32_e32 v108, v108
	v_mul_f32_e32 v102, 0xbfb8aa3b, v102
	v_mul_f32_e32 v109, v97, v96
	v_fma_f32 v96, v101, v161, v161
	v_rcp_f32_e32 v96, v96
	v_fmac_f32_e32 v161, v108, v161
	v_rcp_f32_e32 v97, v161
	v_mul_f32_e32 v43, v47, v43
	v_mul_f32_e32 v101, v98, v96
	v_mul_f32_e32 v96, v103, v99
	v_mul_f32_e32 v99, v96, v97
	v_cvt_pk_bf16_f32 v96, v104, v105
	v_cvt_pk_bf16_f32 v97, v106, v107
	v_cvt_pk_bf16_f32 v98, v100, v109
	v_cvt_pk_bf16_f32 v99, v101, v99
	v_mad_i64_i32 v[100:101], s[24:25], v160, s47, v[112:113]
	v_lshl_add_u64 v[100:101], v[100:101], 0, s[22:23]
	v_lshl_add_u64 v[100:101], v[100:101], 0, s[4:5]
	v_lshl_add_u64 v[100:101], v[100:101], 0, v[136:137]
	global_store_dwordx4 v[100:101], v[96:99], off
	v_mul_f32_e32 v103, v92, v102
	v_exp_f32_e32 v103, v103
	v_mul_f32_e32 v96, v93, v102
	v_exp_f32_e32 v96, v96
	v_mul_f32_e32 v93, v95, v102
	v_exp_f32_e32 v93, v93
	v_fma_f32 v97, v103, v155, v155
	v_fma_f32 v92, v96, v155, v155
	v_mul_f32_e32 v96, v94, v102
	v_rcp_f32_e32 v92, v92
	v_exp_f32_e32 v96, v96
	v_mul_f32_e32 v94, v85, v102
	v_exp_f32_e32 v94, v94
	v_mul_f32_e32 v89, v89, v92
	v_fma_f32 v92, v96, v155, v155
	v_rcp_f32_e32 v92, v92
	v_fma_f32 v93, v93, v155, v155
	v_mul_f32_e32 v85, v86, v102
	v_rcp_f32_e32 v93, v93
	v_mul_f32_e32 v90, v90, v92
	v_mul_f32_e32 v92, v84, v102
	v_exp_f32_e32 v92, v92
	v_exp_f32_e32 v85, v85
	v_mul_f32_e32 v91, v91, v93
	v_rcp_f32_e32 v97, v97
	v_fma_f32 v92, v92, v155, v155
	v_rcp_f32_e32 v92, v92
	v_rsq_f32_e32 v86, v157
	v_mul_f32_e32 v88, v88, v97
	v_mul_f32_e32 v34, v38, v34
	v_mul_f32_e32 v84, v80, v92
	v_fma_f32 v80, v94, v155, v155
	v_rcp_f32_e32 v80, v80
	v_mul_f32_e32 v92, v87, v102
	v_exp_f32_e32 v92, v92
	v_mul_f32_e32 v86, 0xbfb8aa3b, v86
	v_mul_f32_e32 v93, v81, v80
	v_fma_f32 v80, v85, v155, v155
	v_rcp_f32_e32 v80, v80
	v_fmac_f32_e32 v155, v92, v155
	v_rcp_f32_e32 v81, v155
	v_fmamk_f32 v151, v151, 0x3a800000, v170
	v_mul_f32_e32 v85, v82, v80
	v_mul_f32_e32 v80, v87, v83
	v_mul_f32_e32 v83, v80, v81
	v_cvt_pk_bf16_f32 v80, v88, v89
	v_cvt_pk_bf16_f32 v81, v90, v91
	v_cvt_pk_bf16_f32 v82, v84, v93
	v_cvt_pk_bf16_f32 v83, v85, v83
	v_mad_i64_i32 v[84:85], s[24:25], v158, s47, v[112:113]
	v_lshl_add_u64 v[84:85], v[84:85], 0, s[22:23]
	v_lshl_add_u64 v[84:85], v[84:85], 0, s[4:5]
	v_lshl_add_u64 v[84:85], v[84:85], 0, v[136:137]
	global_store_dwordx4 v[84:85], v[80:83], off
	v_mul_f32_e32 v87, v76, v86
	v_exp_f32_e32 v87, v87
	v_mul_f32_e32 v80, v77, v86
	v_exp_f32_e32 v80, v80
	v_mul_f32_e32 v77, v79, v86
	v_exp_f32_e32 v77, v77
	v_fma_f32 v81, v87, v157, v157
	v_fma_f32 v76, v80, v157, v157
	v_mul_f32_e32 v80, v78, v86
	v_rcp_f32_e32 v76, v76
	v_exp_f32_e32 v80, v80
	v_mul_f32_e32 v78, v69, v86
	v_exp_f32_e32 v78, v78
	v_mul_f32_e32 v73, v73, v76
	v_fma_f32 v76, v80, v157, v157
; __device__ __forceinline__ unsigned cvt_pk_bf16(float lo, float hi) { unsigned r; asm volatile("v_cvt_pk_bf16_f32 %0, %1, %2" : "=v"(r) : "v"(lo), "v"(hi)); return r; }
;     __device__ __forceinline__ void operator()(const f32x4 (&acc)[2][2][4][2], const Unit& u, int wr, int wc, int fr, int fq) const {
;     ...
;             for (int m = 0; m < 4; ++m) {
;                 const int row = u.pm * BM + ai * HALF + wr * 64 + m * 16 + fr;
;                 const float x = xv[ai][m], rs = __builtin_amdgcn_rsqf(x);
;                 const float ea = -1.4426950408889634f * rs;
;                 float h[8];
; #pragma unroll
;                 for (int n = 0; n < 2; ++n)
; #pragma unroll
;                     for (int j = 0; j < 4; ++j) {
;                         const float g = acc[ai][0][m][n][j], uu = acc[ai][1][m][n][j];
;                         const float e = __builtin_amdgcn_exp2f(g * ea);
;                         const float q = __builtin_amdgcn_rcpf(__builtin_fmaf(e, x, x));
;                         h[n * 4 + j] = (g * uu) * q;
;                     }
;                 u32x4 w; w.x = cvt_pk_bf16(h[0], h[1]); w.y = cvt_pk_bf16(h[2], h[3]); w.z = cvt_pk_bf16(h[4], h[5]); w.w = cvt_pk_bf16(h[6], h[7]);
;                 *(u32x4*)(Hd + (size_t)row * ldh + u.pn * HALF + wc * 32 + 8 * fq) = w;
	v_rcp_f32_e32 v76, v76
	v_fma_f32 v77, v77, v157, v157
	v_mul_f32_e32 v69, v70, v86
	v_rcp_f32_e32 v77, v77
	v_mul_f32_e32 v74, v74, v76
	v_mul_f32_e32 v76, v68, v86
	v_exp_f32_e32 v76, v76
	v_exp_f32_e32 v69, v69
	v_mul_f32_e32 v75, v75, v77
	v_rcp_f32_e32 v81, v81
	v_fma_f32 v76, v76, v157, v157
	v_rcp_f32_e32 v76, v76
	v_rsq_f32_e32 v70, v159
	v_mul_f32_e32 v72, v72, v81
	v_mul_f32_e32 v24, v28, v24
	v_mul_f32_e32 v68, v64, v76
	v_fma_f32 v64, v78, v157, v157
	v_rcp_f32_e32 v64, v64
	v_mul_f32_e32 v76, v71, v86
	v_exp_f32_e32 v76, v76
	v_mul_f32_e32 v70, 0xbfb8aa3b, v70
	v_mul_f32_e32 v77, v65, v64
	v_fma_f32 v64, v69, v157, v157
	v_rcp_f32_e32 v64, v64
	v_fmac_f32_e32 v157, v76, v157
	v_rcp_f32_e32 v65, v157
	v_mul_f32_e32 v25, v29, v25
	v_mul_f32_e32 v69, v66, v64
	v_mul_f32_e32 v64, v71, v67
	v_mul_f32_e32 v67, v64, v65
	v_cvt_pk_bf16_f32 v64, v72, v73
	v_cvt_pk_bf16_f32 v65, v74, v75
	v_cvt_pk_bf16_f32 v66, v68, v77
	v_cvt_pk_bf16_f32 v67, v69, v67
	v_mad_i64_i32 v[68:69], s[24:25], v156, s47, v[112:113]
	v_lshl_add_u64 v[68:69], v[68:69], 0, s[22:23]
	v_lshl_add_u64 v[68:69], v[68:69], 0, s[4:5]
	v_lshl_add_u64 v[68:69], v[68:69], 0, v[136:137]
	global_store_dwordx4 v[68:69], v[64:67], off
	v_mul_f32_e32 v71, v60, v70
	v_exp_f32_e32 v71, v71
	v_mul_f32_e32 v64, v61, v70
	v_exp_f32_e32 v64, v64
	v_mul_f32_e32 v61, v63, v70
	v_exp_f32_e32 v61, v61
	v_fma_f32 v65, v71, v159, v159
	v_fma_f32 v60, v64, v159, v159
	v_mul_f32_e32 v64, v62, v70
	v_rcp_f32_e32 v60, v60
	v_exp_f32_e32 v64, v64
	v_mul_f32_e32 v62, v53, v70
	v_exp_f32_e32 v62, v62
	v_mul_f32_e32 v57, v57, v60
	v_fma_f32 v60, v64, v159, v159
	v_rcp_f32_e32 v60, v60
	v_fma_f32 v61, v61, v159, v159
	v_mul_f32_e32 v53, v54, v70
	v_rcp_f32_e32 v61, v61
	v_mul_f32_e32 v58, v58, v60
	v_mul_f32_e32 v60, v52, v70
	v_exp_f32_e32 v60, v60
	v_exp_f32_e32 v53, v53
	v_mul_f32_e32 v59, v59, v61
	v_rcp_f32_e32 v65, v65
	v_fma_f32 v60, v60, v159, v159
	v_rcp_f32_e32 v60, v60
	v_rsq_f32_e32 v54, v153
	v_mul_f32_e32 v56, v56, v65
	v_mul_f32_e32 v26, v30, v26
	v_mul_f32_e32 v52, v48, v60
	v_fma_f32 v48, v62, v159, v159
	v_rcp_f32_e32 v48, v48
	v_mul_f32_e32 v60, v55, v70
	v_exp_f32_e32 v60, v60
	v_mul_f32_e32 v54, 0xbfb8aa3b, v54
	v_mul_f32_e32 v61, v49, v48
	v_fma_f32 v48, v53, v159, v159
	v_rcp_f32_e32 v48, v48
	v_fmac_f32_e32 v159, v60, v159
	v_rcp_f32_e32 v49, v159
	v_mul_f32_e32 v16, v20, v16
	v_mul_f32_e32 v53, v50, v48
	v_mul_f32_e32 v48, v55, v51
	v_mul_f32_e32 v51, v48, v49
	v_cvt_pk_bf16_f32 v48, v56, v57
	v_cvt_pk_bf16_f32 v49, v58, v59
	v_cvt_pk_bf16_f32 v50, v52, v61
	v_cvt_pk_bf16_f32 v51, v53, v51
	v_mad_i64_i32 v[52:53], s[24:25], v154, s47, v[112:113]
	v_lshl_add_u64 v[52:53], v[52:53], 0, s[22:23]
	v_lshl_add_u64 v[52:53], v[52:53], 0, s[4:5]
	v_lshl_add_u64 v[52:53], v[52:53], 0, v[136:137]
	global_store_dwordx4 v[52:53], v[48:51], off
	v_mul_f32_e32 v55, v44, v54
	v_exp_f32_e32 v55, v55
	v_mul_f32_e32 v48, v45, v54
	v_exp_f32_e32 v48, v48
	v_mul_f32_e32 v45, v47, v54
	v_exp_f32_e32 v45, v45
	v_fma_f32 v49, v55, v153, v153
	v_fma_f32 v44, v48, v153, v153
	v_mul_f32_e32 v48, v46, v54
	v_rcp_f32_e32 v44, v44
	v_exp_f32_e32 v48, v48
	v_mul_f32_e32 v46, v37, v54
	v_exp_f32_e32 v46, v46
	v_mul_f32_e32 v41, v41, v44
	v_fma_f32 v44, v48, v153, v153
	v_rcp_f32_e32 v44, v44
	v_fma_f32 v45, v45, v153, v153
	v_mul_f32_e32 v37, v38, v54
	v_rcp_f32_e32 v45, v45
	v_mul_f32_e32 v42, v42, v44
	v_mul_f32_e32 v44, v36, v54
	v_exp_f32_e32 v44, v44
	v_exp_f32_e32 v37, v37
	v_mul_f32_e32 v43, v43, v45
	v_rcp_f32_e32 v49, v49
	v_fma_f32 v44, v44, v153, v153
	v_rcp_f32_e32 v44, v44
	v_rsq_f32_e32 v38, v151
	v_mul_f32_e32 v40, v40, v49
	v_mul_f32_e32 v17, v21, v17
	v_mul_f32_e32 v36, v32, v44
	v_fma_f32 v32, v46, v153, v153
	v_rcp_f32_e32 v32, v32
	v_mul_f32_e32 v44, v39, v54
	v_exp_f32_e32 v44, v44
	v_mul_f32_e32 v38, 0xbfb8aa3b, v38
	v_mul_f32_e32 v45, v33, v32
	v_fma_f32 v32, v37, v153, v153
	v_rcp_f32_e32 v32, v32
	v_fmac_f32_e32 v153, v44, v153
; __device__ __forceinline__ unsigned cvt_pk_bf16(float lo, float hi) { unsigned r; asm volatile("v_cvt_pk_bf16_f32 %0, %1, %2" : "=v"(r) : "v"(lo), "v"(hi)); return r; }
; #define PG8_BAR __builtin_amdgcn_s_barrier()
;     __device__ __forceinline__ void operator()(const f32x4 (&acc)[2][2][4][2], const Unit& u, int wr, int wc, int fr, int fq) const {
;     ...
;             for (int m = 0; m < 4; ++m) {
;                 const int row = u.pm * BM + ai * HALF + wr * 64 + m * 16 + fr;
;                 const float x = xv[ai][m], rs = __builtin_amdgcn_rsqf(x);
;                 const float ea = -1.4426950408889634f * rs;
;                 float h[8];
; #pragma unroll
;                 for (int n = 0; n < 2; ++n)
; #pragma unroll
;                     for (int j = 0; j < 4; ++j) {
;                         const float g = acc[ai][0][m][n][j], uu = acc[ai][1][m][n][j];
;                         const float e = __builtin_amdgcn_exp2f(g * ea);
;                         const float q = __builtin_amdgcn_rcpf(__builtin_fmaf(e, x, x));
;                         h[n * 4 + j] = (g * uu) * q;
;                     }
;                 u32x4 w; w.x = cvt_pk_bf16(h[0], h[1]); w.y = cvt_pk_bf16(h[2], h[3]); w.z = cvt_pk_bf16(h[4], h[5]); w.w = cvt_pk_bf16(h[6], h[7]);
;                 *(u32x4*)(Hd + (size_t)row * ldh + u.pn * HALF + wc * 32 + 8 * fq) = w;
; template <class Epi, class Sched, bool ALIGN_EPI = false, bool SP2 = false>
; __device__ __forceinline__ void gemm_phase(PG8_LAS unsigned char* lds, const Gemm g, const Sched& S, const Epi& E, const int wid) {
;     ...
;         if (!has_next) break;
; #pragma unroll
;         for (int a = 0; a < 2; ++a)
; #pragma unroll
;             for (int b = 0; b < 2; ++b)
; #pragma unroll
;                 for (int m = 0; m < 4; ++m)
; #pragma unroll
;                     for (int n = 0; n < 2; ++n) acc[a][b][m][n] = (f32x4){0.f, 0.f, 0.f, 0.f};
;         cur = nxt; cA = nA; cB = nB; ++ui;
;         if constexpr (ALIGN_EPI) { if (wr == 1) PG8_BAR; }
	v_rcp_f32_e32 v33, v153
	v_mul_f32_e32 v27, v31, v27
	v_mul_f32_e32 v37, v34, v32
	v_mul_f32_e32 v32, v39, v35
	v_mul_f32_e32 v35, v32, v33
	v_cvt_pk_bf16_f32 v32, v40, v41
	v_cvt_pk_bf16_f32 v33, v42, v43
	v_cvt_pk_bf16_f32 v34, v36, v45
	v_cvt_pk_bf16_f32 v35, v37, v35
	v_mad_i64_i32 v[36:37], s[24:25], v152, s47, v[112:113]
	v_lshl_add_u64 v[36:37], v[36:37], 0, s[22:23]
	v_lshl_add_u64 v[36:37], v[36:37], 0, s[4:5]
	v_lshl_add_u64 v[36:37], v[36:37], 0, v[136:137]
	global_store_dwordx4 v[36:37], v[32:35], off
	v_mul_f32_e32 v39, v28, v38
	v_exp_f32_e32 v39, v39
	v_mul_f32_e32 v32, v29, v38
	v_exp_f32_e32 v32, v32
	v_mul_f32_e32 v29, v31, v38
	v_exp_f32_e32 v29, v29
	v_fma_f32 v33, v39, v151, v151
	v_fma_f32 v28, v32, v151, v151
	v_mul_f32_e32 v32, v30, v38
	v_rcp_f32_e32 v28, v28
	v_exp_f32_e32 v32, v32
	v_mul_f32_e32 v30, v21, v38
	v_exp_f32_e32 v30, v30
	v_mul_f32_e32 v25, v25, v28
	v_fma_f32 v28, v32, v151, v151
	v_rcp_f32_e32 v28, v28
	v_fma_f32 v29, v29, v151, v151
	v_mul_f32_e32 v21, v22, v38
	v_rcp_f32_e32 v29, v29
	v_mul_f32_e32 v26, v26, v28
	v_mul_f32_e32 v28, v20, v38
	v_exp_f32_e32 v28, v28
	v_exp_f32_e32 v21, v21
	v_mul_f32_e32 v27, v27, v29
	v_rcp_f32_e32 v33, v33
	v_fma_f32 v28, v28, v151, v151
	v_rcp_f32_e32 v28, v28
	v_mul_f32_e32 v18, v22, v18
	v_fmamk_f32 v149, v149, 0x3a800000, v170
	v_rsq_f32_e32 v22, v149
	v_mul_f32_e32 v20, v16, v28
	v_fma_f32 v16, v30, v151, v151
	v_rcp_f32_e32 v16, v16
	v_mul_f32_e32 v28, v23, v38
	v_exp_f32_e32 v28, v28
	v_mul_f32_e32 v24, v24, v33
	v_mul_f32_e32 v29, v17, v16
	v_fma_f32 v16, v21, v151, v151
	v_rcp_f32_e32 v16, v16
	v_fmac_f32_e32 v151, v28, v151
	v_rcp_f32_e32 v17, v151
	v_mul_f32_e32 v22, 0xbfb8aa3b, v22
	v_mul_f32_e32 v21, v18, v16
	v_mul_f32_e32 v16, v23, v19
	v_mul_f32_e32 v19, v16, v17
	v_cvt_pk_bf16_f32 v16, v24, v25
	v_cvt_pk_bf16_f32 v17, v26, v27
	v_cvt_pk_bf16_f32 v18, v20, v29
	v_cvt_pk_bf16_f32 v19, v21, v19
	v_mad_i64_i32 v[20:21], s[24:25], v150, s47, v[112:113]
	v_lshl_add_u64 v[20:21], v[20:21], 0, s[22:23]
	v_lshl_add_u64 v[20:21], v[20:21], 0, s[4:5]
	v_lshl_add_u64 v[20:21], v[20:21], 0, v[136:137]
	global_store_dwordx4 v[20:21], v[16:19], off
	v_mul_f32_e32 v23, v12, v22
	v_mul_f32_e32 v8, v12, v8
	v_mul_f32_e32 v16, v13, v22
	v_exp_f32_e32 v16, v16
	v_mul_f32_e32 v9, v13, v9
	v_mul_f32_e32 v10, v14, v10
	v_mul_f32_e32 v13, v15, v22
	v_fma_f32 v12, v16, v149, v149
	v_mul_f32_e32 v16, v14, v22
	v_rcp_f32_e32 v12, v12
	v_exp_f32_e32 v16, v16
	v_mul_f32_e32 v14, v5, v22
	v_exp_f32_e32 v13, v13
	v_mul_f32_e32 v9, v9, v12
	v_fma_f32 v12, v16, v149, v149
	v_rcp_f32_e32 v12, v12
	v_exp_f32_e32 v14, v14
	v_mul_f32_e32 v0, v4, v0
	v_fma_f32 v13, v13, v149, v149
	v_mul_f32_e32 v10, v10, v12
	v_mul_f32_e32 v12, v4, v22
	v_exp_f32_e32 v12, v12
	v_mul_f32_e32 v1, v5, v1
	v_mul_f32_e32 v5, v6, v22
	v_rcp_f32_e32 v13, v13
	v_fma_f32 v12, v12, v149, v149
	v_rcp_f32_e32 v12, v12
	v_exp_f32_e32 v5, v5
	v_exp_f32_e32 v23, v23
	v_mul_f32_e32 v11, v15, v11
	v_mul_f32_e32 v4, v0, v12
	v_fma_f32 v0, v14, v149, v149
	v_rcp_f32_e32 v0, v0
	v_mul_f32_e32 v12, v7, v22
	v_exp_f32_e32 v12, v12
	v_mul_f32_e32 v11, v11, v13
	v_mul_f32_e32 v13, v1, v0
	v_fma_f32 v0, v5, v149, v149
	v_fma_f32 v17, v23, v149, v149
	v_rcp_f32_e32 v0, v0
	v_fmac_f32_e32 v149, v12, v149
	v_rcp_f32_e32 v1, v149
	v_rcp_f32_e32 v17, v17
	v_mul_f32_e32 v2, v6, v2
	v_mul_f32_e32 v5, v2, v0
	v_mul_f32_e32 v0, v7, v3
	v_mul_f32_e32 v3, v0, v1
	v_mul_f32_e32 v8, v8, v17
	v_cvt_pk_bf16_f32 v0, v8, v9
	v_cvt_pk_bf16_f32 v1, v10, v11
	v_cvt_pk_bf16_f32 v2, v4, v13
	v_cvt_pk_bf16_f32 v3, v5, v3
	v_mad_i64_i32 v[4:5], s[24:25], v148, s47, v[112:113]
	v_lshl_add_u64 v[4:5], v[4:5], 0, s[22:23]
	v_lshl_add_u64 v[4:5], v[4:5], 0, s[4:5]
	v_lshl_add_u64 v[4:5], v[4:5], 0, v[136:137]
	s_andn2_b64 vcc, exec, s[2:3]
	s_mov_b64 s[2:3], -1
	global_store_dwordx4 v[4:5], v[0:3], off
	s_cbranch_vccnz .LBB0_1863
	s_andn2_b64 vcc, exec, s[6:7]
	s_cbranch_vccnz .LBB0_1862
	s_barrier
	s_branch .LBB0_1862

; #define PG8_STAGE(bufoff, gbase, voff) do { _Pragma("unroll") for (int _i = 0; _i < 2; ++_i) \
;         __builtin_amdgcn_global_load_lds((const unsigned*)((const char*)(gbase) + (voff)[_i]), (PG8_LAS unsigned*)(lds + (bufoff) + ldsw + _i * 8192), 16, 0, 0); } while (0)
; #define PG8_LDA(dst, b, h) do { _Pragma("unroll") for (int m = 0; m < 4; ++m) _Pragma("unroll") for (int k = 0; k < 2; ++k) dst[m][k] = *(const PG8_LAS bf16x8*)(lds + PG8_SA(b, h) + aoff + m * 2048 + k * 1024); } while (0)
; #define PG8_LDB(dst, b, h) do { _Pragma("unroll") for (int n = 0; n < 2; ++n) _Pragma("unroll") for (int k = 0; k < 2; ++k) dst[n][k] = *(const PG8_LAS bf16x8*)(lds + PG8_SB(b, h) + boff + n * 2048 + k * 1024); } while (0)
; #define PG8_WAIT_V(n) asm volatile("s_waitcnt vmcnt(" #n ")" ::: "memory")
; #define PG8_BAR __builtin_amdgcn_s_barrier()
;     __device__ __forceinline__ void operator()(const f32x4 (&acc)[2][2][4][2], const Unit& u, int wr, int wc, int fr, int fq) const {
;     ...
;             f32x4 qd[2][4];
; #pragma unroll
;             for (int ai = 0; ai < 2; ++ai)
; #pragma unroll
;                 for (int m = 0; m < 4; ++m) qd[ai][m] = row_quad(ssq, u.pm * BM + ai * HALF + wr * 64 + m * 16 + fr, fq);
; template <class Epi, class Sched, bool ALIGN_EPI = false, bool SP2 = false>
; __device__ __forceinline__ void gemm_phase(PG8_LAS unsigned char* lds, const Gemm g, const Sched& S, const Epi& E, const int wid) {
;     ...
;         for (int t = 0; t < nt; t += 2) {
;             const bool last = (t == nt - 2);
;             const char* a1 = cA + (size_t)(t + 1) * kstep;
;             const char* a2 = last ? nA : cA + (size_t)(t + 2) * kstep; const char* b2 = last ? nB : cB + (size_t)(t + 2) * kstep;
;             const char* a3 = a2 + kstep; const char* b3 = b2 + kstep;
;             if (last && has_next) S.a_ready(nxt);
;             if constexpr (SP2) {
;             PG8_LDB(B0, 0, 0); PG8_LDB(B1, 0, 1); PG8_SCHED; PG8_LDA(At, 0, 0); PG8_STAGE(PG8_SA(1, 1), a1 + hstepA, voffA);
;             PG8_WAIT_V(8); PG8_WAIT_L(0); PG8_BAR; PG8_MMA(0, 0, At, B0); PG8_MMA(0, 1, At, B1); PG8_BAR; PG8_SCHED;
;             PG8_LDA(At, 0, 1); PG8_STAGE(PG8_SB(0, 0), b2, voffB); PG8_STAGE(PG8_SB(0, 1), b2 + hstepB, voffB); PG8_STAGE(PG8_SA(0, 0), a2, voffA);
;             PG8_WAIT_V(8); PG8_WAIT_L(0); PG8_BAR; PG8_MMA(1, 0, At, B0); PG8_MMA(1, 1, At, B1); PG8_BAR; PG8_SCHED;
.LBB0_2811:
	s_ashr_i32 s17, s16, 31
	s_lshl_b64 s[18:19], s[16:17], 19
	s_add_u32 s18, s0, s18
	s_addc_u32 s19, s1, s19
	s_and_b64 s[20:21], s[2:3], exec
	s_cselect_b32 s17, s19, s25
	s_cselect_b32 s47, s18, s24
	s_ashr_i32 s15, s14, 31
	s_lshl_b64 s[20:21], s[14:15], 19
	s_add_u32 s20, s30, s20
	s_addc_u32 s21, s31, s21
	s_and_b64 s[28:29], s[2:3], exec
	s_cselect_b32 s15, s21, s27
	s_cselect_b32 s48, s20, s26
	s_add_u32 s24, s24, 0x40080
	s_addc_u32 s25, s25, 0
	s_add_u32 s49, s26, 0x100
	s_addc_u32 s56, s27, 0
	s_mov_b32 s57, -2
	v_add_u32_e32 v252, 0x18000, v165
	v_add_u32_e32 v253, 0x1c000, v165
	ds_read_b128 v[148:151], v166
	ds_read_b128 v[152:155], v166 offset:1024
	ds_read_b128 v[156:159], v166 offset:2048
	ds_read_b128 v[160:163], v166 offset:3072
	ds_read_b128 v[172:175], v167
	ds_read_b128 v[176:179], v167 offset:1024
	ds_read_b128 v[180:183], v167 offset:2048
	ds_read_b128 v[184:187], v167 offset:3072
	s_add_u32 s26, s24, 0xfffc0080
	s_addc_u32 s27, s25, -1
	s_cmp_eq_u32 s57, 12
	s_cselect_b32 s29, s17, s27
	s_cselect_b32 s28, s47, s26
	s_cselect_b32 s27, s15, s56
	s_cselect_b32 s26, s48, s49
	s_add_i32 m0, s36, 0xc000
	ds_read_b128 v[188:191], v168
	ds_read_b128 v[192:195], v168 offset:1024
	ds_read_b128 v[196:199], v168 offset:2048
	ds_read_b128 v[200:203], v168 offset:3072
	ds_read_b128 v[204:207], v168 offset:4096
	ds_read_b128 v[208:211], v168 offset:5120
	ds_read_b128 v[212:215], v168 offset:6144
	ds_read_b128 v[216:219], v168 offset:7168
	global_load_lds_dwordx4 v140, s[24:25]
	s_add_i32 m0, s36, 0xe000
	s_nop 0
	global_load_lds_dwordx4 v142, s[24:25]
	s_waitcnt vmcnt(8) lgkmcnt(0)
	v_lshl_add_u32 v220, s22, 8, v164
	v_add_u32_e32 v236, 0x80, v220
	v_ashrrev_i32_e32 v221, 31, v220
	v_ashrrev_i32_e32 v237, 31, v236
	v_lshlrev_b64 v[220:221], 6, v[220:221]
	v_lshlrev_b64 v[236:237], 6, v[236:237]
	v_lshl_add_u64 v[220:221], v[138:139], 0, v[220:221]
	v_lshl_add_u64 v[236:237], v[138:139], 0, v[236:237]
	global_load_dwordx4 v[224:227], v[220:221], off offset:1024
	global_load_dwordx4 v[228:231], v[220:221], off offset:2048
	global_load_dwordx4 v[232:235], v[220:221], off offset:3072
	global_load_dwordx4 v[240:243], v[236:237], off offset:1024
	global_load_dwordx4 v[244:247], v[236:237], off offset:2048
	global_load_dwordx4 v[248:251], v[236:237], off offset:3072
	s_nop 0
	global_load_dwordx4 v[220:223], v[220:221], off
	s_nop 0
	global_load_dwordx4 v[236:239], v[236:237], off
	s_barrier
	s_setprio 1
	v_mfma_f32_16x16x32_bf16 v[124:127], v[148:151], v[188:191], 0
	v_mfma_f32_16x16x32_bf16 v[116:119], v[156:159], v[188:191], 0
	v_mfma_f32_16x16x32_bf16 v[108:111], v[148:151], v[196:199], 0
	v_mfma_f32_16x16x32_bf16 v[100:103], v[156:159], v[196:199], 0
	v_mfma_f32_16x16x32_bf16 v[92:95], v[148:151], v[204:207], 0
	v_mfma_f32_16x16x32_bf16 v[84:87], v[156:159], v[204:207], 0
	v_mfma_f32_16x16x32_bf16 v[76:79], v[148:151], v[212:215], 0
	v_mfma_f32_16x16x32_bf16 v[68:71], v[156:159], v[212:215], 0
	v_mfma_f32_16x16x32_bf16 v[124:127], v[152:155], v[192:195], v[124:127]
	v_mfma_f32_16x16x32_bf16 v[116:119], v[160:163], v[192:195], v[116:119]
	v_mfma_f32_16x16x32_bf16 v[108:111], v[152:155], v[200:203], v[108:111]
	v_mfma_f32_16x16x32_bf16 v[100:103], v[160:163], v[200:203], v[100:103]
	v_mfma_f32_16x16x32_bf16 v[92:95], v[152:155], v[208:211], v[92:95]
	v_mfma_f32_16x16x32_bf16 v[84:87], v[160:163], v[208:211], v[84:87]
	v_mfma_f32_16x16x32_bf16 v[76:79], v[152:155], v[216:219], v[76:79]
	v_mfma_f32_16x16x32_bf16 v[68:71], v[160:163], v[216:219], v[68:71]
	s_setprio 0
	s_setprio 1
	v_mfma_f32_16x16x32_bf16 v[120:123], v[172:175], v[188:191], 0
	v_mfma_f32_16x16x32_bf16 v[112:115], v[180:183], v[188:191], 0
	v_mfma_f32_16x16x32_bf16 v[104:107], v[172:175], v[196:199], 0
	v_mfma_f32_16x16x32_bf16 v[96:99], v[180:183], v[196:199], 0
	v_mfma_f32_16x16x32_bf16 v[88:91], v[172:175], v[204:207], 0
	v_mfma_f32_16x16x32_bf16 v[80:83], v[180:183], v[204:207], 0
	v_mfma_f32_16x16x32_bf16 v[72:75], v[172:175], v[212:215], 0
	v_mfma_f32_16x16x32_bf16 v[64:67], v[180:183], v[212:215], 0
	v_mfma_f32_16x16x32_bf16 v[120:123], v[176:179], v[192:195], v[120:123]
	v_mfma_f32_16x16x32_bf16 v[112:115], v[184:187], v[192:195], v[112:115]
	v_mfma_f32_16x16x32_bf16 v[104:107], v[176:179], v[200:203], v[104:107]
	v_mfma_f32_16x16x32_bf16 v[96:99], v[184:187], v[200:203], v[96:99]
	v_mfma_f32_16x16x32_bf16 v[88:91], v[176:179], v[208:211], v[88:91]
	v_mfma_f32_16x16x32_bf16 v[80:83], v[184:187], v[208:211], v[80:83]
	v_mfma_f32_16x16x32_bf16 v[72:75], v[176:179], v[216:219], v[72:75]
	v_mfma_f32_16x16x32_bf16 v[64:67], v[184:187], v[216:219], v[64:67]
	s_setprio 0
	s_barrier
	s_add_i32 s58, s43, s33
	s_add_u32 s98, s26, 0x80
	s_addc_u32 s99, s27, 0
	s_mov_b32 m0, s58
	ds_read_b128 v[188:191], v168 offset:16384
	ds_read_b128 v[192:195], v168 offset:17408
	ds_read_b128 v[196:199], v168 offset:18432
	ds_read_b128 v[200:203], v168 offset:19456
	ds_read_b128 v[204:207], v168 offset:20480
	ds_read_b128 v[208:211], v168 offset:21504
	ds_read_b128 v[212:215], v168 offset:22528
	ds_read_b128 v[216:219], v168 offset:23552
	global_load_lds_dwordx4 v132, s[26:27]
	s_add_i32 m0, s58, 0x2000
	s_add_u32 s58, s26, 0x40000
	s_addc_u32 s59, s27, 0
	s_add_i32 s60, s44, s33
	global_load_lds_dwordx4 v128, s[26:27]
	s_mov_b32 m0, s60
	s_add_u32 s100, s28, 0x80
	s_addc_u32 s101, s29, 0
	global_load_lds_dwordx4 v132, s[58:59]
	s_add_i32 m0, s60, 0x2000
	s_nop 0
	global_load_lds_dwordx4 v128, s[58:59]
	s_mov_b32 m0, s36
	s_nop 0
	global_load_lds_dwordx4 v134, s[28:29]
	s_mov_b32 m0, s37
	s_nop 0
	global_load_lds_dwordx4 v130, s[28:29]
	s_waitcnt vmcnt(8) lgkmcnt(0)
	s_barrier
; #define PG8_STAGE(bufoff, gbase, voff) do { _Pragma("unroll") for (int _i = 0; _i < 2; ++_i) \
;         __builtin_amdgcn_global_load_lds((const unsigned*)((const char*)(gbase) + (voff)[_i]), (PG8_LAS unsigned*)(lds + (bufoff) + ldsw + _i * 8192), 16, 0, 0); } while (0)
; #define PG8_LDA(dst, b, h) do { _Pragma("unroll") for (int m = 0; m < 4; ++m) _Pragma("unroll") for (int k = 0; k < 2; ++k) dst[m][k] = *(const PG8_LAS bf16x8*)(lds + PG8_SA(b, h) + aoff + m * 2048 + k * 1024); } while (0)
; #define PG8_LDB(dst, b, h) do { _Pragma("unroll") for (int n = 0; n < 2; ++n) _Pragma("unroll") for (int k = 0; k < 2; ++k) dst[n][k] = *(const PG8_LAS bf16x8*)(lds + PG8_SB(b, h) + boff + n * 2048 + k * 1024); } while (0)
; #define PG8_MMA(ai, bj, At, Bt) do { __builtin_amdgcn_s_setprio(1); _Pragma("unroll") for (int m = 0; m < 4; ++m) _Pragma("unroll") for (int n = 0; n < 2; ++n) _Pragma("unroll") for (int k = 0; k < 2; ++k) \
;         acc[ai][bj][m][n] = __builtin_amdgcn_mfma_f32_16x16x32_bf16(Bt[n][k], At[m][k], acc[ai][bj][m][n], 0, 0, 0); __builtin_amdgcn_s_setprio(0); } while (0)
; #define PG8_WAIT_V(n) asm volatile("s_waitcnt vmcnt(" #n ")" ::: "memory")
; #define PG8_WAIT_L(n) asm volatile("s_waitcnt lgkmcnt(" #n ")" ::: "memory")
; #define PG8_BAR __builtin_amdgcn_s_barrier()
; #define PG8_SCHED __builtin_amdgcn_sched_barrier(0)
; template <class Epi, class Sched, bool ALIGN_EPI = false, bool SP2 = false>
; __device__ __forceinline__ void gemm_phase(PG8_LAS unsigned char* lds, const Gemm g, const Sched& S, const Epi& E, const int wid) {
;     ...
;             PG8_LDB(B0, 0, 0); PG8_LDB(B1, 0, 1); PG8_SCHED; PG8_LDA(At, 0, 0); PG8_STAGE(PG8_SA(1, 1), a1 + hstepA, voffA);
;             PG8_WAIT_V(8); PG8_WAIT_L(0); PG8_BAR; PG8_MMA(0, 0, At, B0); PG8_MMA(0, 1, At, B1); PG8_BAR; PG8_SCHED;
;             PG8_LDA(At, 0, 1); PG8_STAGE(PG8_SB(0, 0), b2, voffB); PG8_STAGE(PG8_SB(0, 1), b2 + hstepB, voffB); PG8_STAGE(PG8_SA(0, 0), a2, voffA);
;             PG8_WAIT_V(8); PG8_WAIT_L(0); PG8_BAR; PG8_MMA(1, 0, At, B0); PG8_MMA(1, 1, At, B1); PG8_BAR; PG8_SCHED;
;             PG8_LDB(B0, 1, 0); PG8_LDB(B1, 1, 1); PG8_SCHED; PG8_LDA(At, 1, 0); PG8_STAGE(PG8_SA(0, 1), a2 + hstepA, voffA);
;             PG8_WAIT_V(8); PG8_WAIT_L(0); PG8_BAR; PG8_MMA(0, 0, At, B0); PG8_MMA(0, 1, At, B1); PG8_BAR; PG8_SCHED;
	s_setprio 1
	v_mfma_f32_16x16x32_bf16 v[60:63], v[148:151], v[188:191], 0
	v_mfma_f32_16x16x32_bf16 v[52:55], v[156:159], v[188:191], 0
	v_mfma_f32_16x16x32_bf16 v[44:47], v[148:151], v[196:199], 0
	v_mfma_f32_16x16x32_bf16 v[36:39], v[156:159], v[196:199], 0
	v_mfma_f32_16x16x32_bf16 v[28:31], v[148:151], v[204:207], 0
	v_mfma_f32_16x16x32_bf16 v[20:23], v[156:159], v[204:207], 0
	v_mfma_f32_16x16x32_bf16 v[12:15], v[148:151], v[212:215], 0
	v_mfma_f32_16x16x32_bf16 v[4:7], v[156:159], v[212:215], 0
	v_mfma_f32_16x16x32_bf16 v[60:63], v[152:155], v[192:195], v[60:63]
	v_mfma_f32_16x16x32_bf16 v[52:55], v[160:163], v[192:195], v[52:55]
	v_mfma_f32_16x16x32_bf16 v[44:47], v[152:155], v[200:203], v[44:47]
	v_mfma_f32_16x16x32_bf16 v[36:39], v[160:163], v[200:203], v[36:39]
	v_mfma_f32_16x16x32_bf16 v[28:31], v[152:155], v[208:211], v[28:31]
	v_mfma_f32_16x16x32_bf16 v[20:23], v[160:163], v[208:211], v[20:23]
	v_mfma_f32_16x16x32_bf16 v[12:15], v[152:155], v[216:219], v[12:15]
	v_mfma_f32_16x16x32_bf16 v[4:7], v[160:163], v[216:219], v[4:7]
	s_setprio 0
	s_setprio 1
	v_mfma_f32_16x16x32_bf16 v[56:59], v[172:175], v[188:191], 0
	v_mfma_f32_16x16x32_bf16 v[48:51], v[180:183], v[188:191], 0
	v_mfma_f32_16x16x32_bf16 v[40:43], v[172:175], v[196:199], 0
	v_mfma_f32_16x16x32_bf16 v[32:35], v[180:183], v[196:199], 0
	v_mfma_f32_16x16x32_bf16 v[24:27], v[172:175], v[204:207], 0
	v_mfma_f32_16x16x32_bf16 v[16:19], v[180:183], v[204:207], 0
	v_mfma_f32_16x16x32_bf16 v[8:11], v[172:175], v[212:215], 0
	v_mfma_f32_16x16x32_bf16 v[0:3], v[180:183], v[212:215], 0
	v_mfma_f32_16x16x32_bf16 v[56:59], v[176:179], v[192:195], v[56:59]
	v_mfma_f32_16x16x32_bf16 v[48:51], v[184:187], v[192:195], v[48:51]
	v_mfma_f32_16x16x32_bf16 v[40:43], v[176:179], v[200:203], v[40:43]
	v_mfma_f32_16x16x32_bf16 v[32:35], v[184:187], v[200:203], v[32:35]
	v_mfma_f32_16x16x32_bf16 v[24:27], v[176:179], v[208:211], v[24:27]
	v_mfma_f32_16x16x32_bf16 v[16:19], v[184:187], v[208:211], v[16:19]
	v_mfma_f32_16x16x32_bf16 v[8:11], v[176:179], v[216:219], v[8:11]
	v_mfma_f32_16x16x32_bf16 v[0:3], v[184:187], v[216:219], v[0:3]
	s_setprio 0
	s_barrier
	s_add_i32 s58, 0, 0x18000
	s_add_i32 s59, 0, 0x1c000
	ds_read_b128 v[148:151], v252
	ds_read_b128 v[152:155], v252 offset:1024
	ds_read_b128 v[156:159], v252 offset:2048
	ds_read_b128 v[160:163], v252 offset:3072
	ds_read_b128 v[172:175], v253
	ds_read_b128 v[176:179], v253 offset:1024
	ds_read_b128 v[180:183], v253 offset:2048
	ds_read_b128 v[184:187], v253 offset:3072
	s_add_u32 s28, s28, 0x40000
	s_addc_u32 s29, s29, 0
	s_mov_b32 m0, s38
	ds_read_b128 v[188:191], v168 offset:32768
	ds_read_b128 v[192:195], v168 offset:33792
	ds_read_b128 v[196:199], v168 offset:34816
	ds_read_b128 v[200:203], v168 offset:35840
	ds_read_b128 v[204:207], v168 offset:36864
	ds_read_b128 v[208:211], v168 offset:37888
	ds_read_b128 v[212:215], v168 offset:38912
	ds_read_b128 v[216:219], v168 offset:39936
	global_load_lds_dwordx4 v134, s[28:29]
	s_mov_b32 m0, s39
	s_nop 0
	global_load_lds_dwordx4 v130, s[28:29]
	s_waitcnt vmcnt(8) lgkmcnt(0)
	s_barrier
	s_setprio 1
	v_mfma_f32_16x16x32_bf16 v[124:127], v[148:151], v[188:191], v[124:127]
	v_mfma_f32_16x16x32_bf16 v[116:119], v[156:159], v[188:191], v[116:119]
	v_mfma_f32_16x16x32_bf16 v[108:111], v[148:151], v[196:199], v[108:111]
	v_mfma_f32_16x16x32_bf16 v[100:103], v[156:159], v[196:199], v[100:103]
	v_mfma_f32_16x16x32_bf16 v[92:95], v[148:151], v[204:207], v[92:95]
	v_mfma_f32_16x16x32_bf16 v[84:87], v[156:159], v[204:207], v[84:87]
	v_mfma_f32_16x16x32_bf16 v[76:79], v[148:151], v[212:215], v[76:79]
	v_mfma_f32_16x16x32_bf16 v[68:71], v[156:159], v[212:215], v[68:71]
	v_mfma_f32_16x16x32_bf16 v[124:127], v[152:155], v[192:195], v[124:127]
	v_mfma_f32_16x16x32_bf16 v[116:119], v[160:163], v[192:195], v[116:119]
	v_mfma_f32_16x16x32_bf16 v[108:111], v[152:155], v[200:203], v[108:111]
	v_mfma_f32_16x16x32_bf16 v[100:103], v[160:163], v[200:203], v[100:103]
	v_mfma_f32_16x16x32_bf16 v[92:95], v[152:155], v[208:211], v[92:95]
	v_mfma_f32_16x16x32_bf16 v[84:87], v[160:163], v[208:211], v[84:87]
	v_mfma_f32_16x16x32_bf16 v[76:79], v[152:155], v[216:219], v[76:79]
	v_mfma_f32_16x16x32_bf16 v[68:71], v[160:163], v[216:219], v[68:71]
	s_setprio 0
	s_setprio 1
	v_mfma_f32_16x16x32_bf16 v[120:123], v[172:175], v[188:191], v[120:123]
	v_mfma_f32_16x16x32_bf16 v[112:115], v[180:183], v[188:191], v[112:115]
	v_mfma_f32_16x16x32_bf16 v[104:107], v[172:175], v[196:199], v[104:107]
	v_mfma_f32_16x16x32_bf16 v[96:99], v[180:183], v[196:199], v[96:99]
	v_mfma_f32_16x16x32_bf16 v[88:91], v[172:175], v[204:207], v[88:91]
	v_mfma_f32_16x16x32_bf16 v[80:83], v[180:183], v[204:207], v[80:83]
	v_mfma_f32_16x16x32_bf16 v[72:75], v[172:175], v[212:215], v[72:75]
	v_mfma_f32_16x16x32_bf16 v[64:67], v[180:183], v[212:215], v[64:67]
	v_mfma_f32_16x16x32_bf16 v[120:123], v[176:179], v[192:195], v[120:123]
	v_mfma_f32_16x16x32_bf16 v[112:115], v[184:187], v[192:195], v[112:115]
	v_mfma_f32_16x16x32_bf16 v[104:107], v[176:179], v[200:203], v[104:107]
	v_mfma_f32_16x16x32_bf16 v[96:99], v[184:187], v[200:203], v[96:99]
	v_mfma_f32_16x16x32_bf16 v[88:91], v[176:179], v[208:211], v[88:91]
	v_mfma_f32_16x16x32_bf16 v[80:83], v[184:187], v[208:211], v[80:83]
	v_mfma_f32_16x16x32_bf16 v[72:75], v[176:179], v[216:219], v[72:75]
	v_mfma_f32_16x16x32_bf16 v[64:67], v[184:187], v[216:219], v[64:67]
	s_setprio 0
	s_barrier
; #define PG8_STAGE(bufoff, gbase, voff) do { _Pragma("unroll") for (int _i = 0; _i < 2; ++_i) \
;         __builtin_amdgcn_global_load_lds((const unsigned*)((const char*)(gbase) + (voff)[_i]), (PG8_LAS unsigned*)(lds + (bufoff) + ldsw + _i * 8192), 16, 0, 0); } while (0)
; #define PG8_LDA(dst, b, h) do { _Pragma("unroll") for (int m = 0; m < 4; ++m) _Pragma("unroll") for (int k = 0; k < 2; ++k) dst[m][k] = *(const PG8_LAS bf16x8*)(lds + PG8_SA(b, h) + aoff + m * 2048 + k * 1024); } while (0)
; #define PG8_MMA(ai, bj, At, Bt) do { __builtin_amdgcn_s_setprio(1); _Pragma("unroll") for (int m = 0; m < 4; ++m) _Pragma("unroll") for (int n = 0; n < 2; ++n) _Pragma("unroll") for (int k = 0; k < 2; ++k) \
;         acc[ai][bj][m][n] = __builtin_amdgcn_mfma_f32_16x16x32_bf16(Bt[n][k], At[m][k], acc[ai][bj][m][n], 0, 0, 0); __builtin_amdgcn_s_setprio(0); } while (0)
; #define PG8_WAIT_V(n) asm volatile("s_waitcnt vmcnt(" #n ")" ::: "memory")
; #define PG8_WAIT_L(n) asm volatile("s_waitcnt lgkmcnt(" #n ")" ::: "memory")
; #define PG8_BAR __builtin_amdgcn_s_barrier()
; #define PG8_SCHED __builtin_amdgcn_sched_barrier(0)
; template <class Epi, class Sched, bool ALIGN_EPI = false, bool SP2 = false>
; __device__ __forceinline__ void gemm_phase(PG8_LAS unsigned char* lds, const Gemm g, const Sched& S, const Epi& E, const int wid) {
;     ...
;         for (int t = 0; t < nt; t += 2) {
;             const bool last = (t == nt - 2);
;             const char* a1 = cA + (size_t)(t + 1) * kstep;
;             const char* a2 = last ? nA : cA + (size_t)(t + 2) * kstep; const char* b2 = last ? nB : cB + (size_t)(t + 2) * kstep;
;             const char* a3 = a2 + kstep; const char* b3 = b2 + kstep;
;             if (last && has_next) S.a_ready(nxt);
;     ...
;             PG8_LDA(At, 1, 1); PG8_STAGE(PG8_SB(1, 0), b3, voffB); PG8_STAGE(PG8_SB(1, 1), b3 + hstepB, voffB); PG8_STAGE(PG8_SA(1, 0), a3, voffA);
;             PG8_WAIT_V(8); PG8_WAIT_L(0); PG8_BAR; PG8_MMA(1, 0, At, B0); PG8_MMA(1, 1, At, B1); PG8_BAR; PG8_SCHED;
	s_add_i32 s28, s58, s33
	s_mov_b32 m0, s28
	ds_read_b128 v[188:191], v168 offset:49152
	ds_read_b128 v[192:195], v168 offset:50176
	ds_read_b128 v[196:199], v168 offset:51200
	ds_read_b128 v[200:203], v168 offset:52224
	ds_read_b128 v[204:207], v168 offset:53248
	ds_read_b128 v[208:211], v168 offset:54272
	ds_read_b128 v[212:215], v168 offset:55296
	ds_read_b128 v[216:219], v168 offset:56320
	global_load_lds_dwordx4 v132, s[98:99]
	s_add_i32 m0, s28, 0x2000
	s_add_u32 s26, s26, 0x40080
	s_addc_u32 s27, s27, 0
	s_add_i32 s28, s59, s33
	global_load_lds_dwordx4 v128, s[98:99]
	s_mov_b32 m0, s28
	s_nop 0
	global_load_lds_dwordx4 v132, s[26:27]
	s_add_i32 m0, s28, 0x2000
	s_nop 0
	global_load_lds_dwordx4 v128, s[26:27]
	s_mov_b32 m0, s40
	s_nop 0
	global_load_lds_dwordx4 v134, s[100:101]
	s_mov_b32 m0, s41
	s_nop 0
	global_load_lds_dwordx4 v130, s[100:101]
	s_waitcnt vmcnt(8) lgkmcnt(0)
	s_barrier
	s_setprio 1
	v_mfma_f32_16x16x32_bf16 v[60:63], v[148:151], v[188:191], v[60:63]
	v_mfma_f32_16x16x32_bf16 v[52:55], v[156:159], v[188:191], v[52:55]
	v_mfma_f32_16x16x32_bf16 v[44:47], v[148:151], v[196:199], v[44:47]
	v_mfma_f32_16x16x32_bf16 v[36:39], v[156:159], v[196:199], v[36:39]
	v_mfma_f32_16x16x32_bf16 v[28:31], v[148:151], v[204:207], v[28:31]
	v_mfma_f32_16x16x32_bf16 v[20:23], v[156:159], v[204:207], v[20:23]
	v_mfma_f32_16x16x32_bf16 v[12:15], v[148:151], v[212:215], v[12:15]
	v_mfma_f32_16x16x32_bf16 v[4:7], v[156:159], v[212:215], v[4:7]
	v_mfma_f32_16x16x32_bf16 v[60:63], v[152:155], v[192:195], v[60:63]
	v_mfma_f32_16x16x32_bf16 v[52:55], v[160:163], v[192:195], v[52:55]
	v_mfma_f32_16x16x32_bf16 v[44:47], v[152:155], v[200:203], v[44:47]
	v_mfma_f32_16x16x32_bf16 v[36:39], v[160:163], v[200:203], v[36:39]
	v_mfma_f32_16x16x32_bf16 v[28:31], v[152:155], v[208:211], v[28:31]
	v_mfma_f32_16x16x32_bf16 v[20:23], v[160:163], v[208:211], v[20:23]
	v_mfma_f32_16x16x32_bf16 v[12:15], v[152:155], v[216:219], v[12:15]
	v_mfma_f32_16x16x32_bf16 v[4:7], v[160:163], v[216:219], v[4:7]
	s_setprio 0
	s_setprio 1
	v_mfma_f32_16x16x32_bf16 v[56:59], v[172:175], v[188:191], v[56:59]
	v_mfma_f32_16x16x32_bf16 v[48:51], v[180:183], v[188:191], v[48:51]
	v_mfma_f32_16x16x32_bf16 v[40:43], v[172:175], v[196:199], v[40:43]
	v_mfma_f32_16x16x32_bf16 v[32:35], v[180:183], v[196:199], v[32:35]
	v_mfma_f32_16x16x32_bf16 v[24:27], v[172:175], v[204:207], v[24:27]
	v_mfma_f32_16x16x32_bf16 v[16:19], v[180:183], v[204:207], v[16:19]
	v_mfma_f32_16x16x32_bf16 v[8:11], v[172:175], v[212:215], v[8:11]
	v_mfma_f32_16x16x32_bf16 v[0:3], v[180:183], v[212:215], v[0:3]
	v_mfma_f32_16x16x32_bf16 v[56:59], v[176:179], v[192:195], v[56:59]
	v_mfma_f32_16x16x32_bf16 v[48:51], v[184:187], v[192:195], v[48:51]
	v_mfma_f32_16x16x32_bf16 v[40:43], v[176:179], v[200:203], v[40:43]
	v_mfma_f32_16x16x32_bf16 v[32:35], v[184:187], v[200:203], v[32:35]
	v_mfma_f32_16x16x32_bf16 v[24:27], v[176:179], v[208:211], v[24:27]
	v_mfma_f32_16x16x32_bf16 v[16:19], v[184:187], v[208:211], v[16:19]
	v_mfma_f32_16x16x32_bf16 v[8:11], v[176:179], v[216:219], v[8:11]
	v_mfma_f32_16x16x32_bf16 v[0:3], v[184:187], v[216:219], v[0:3]
	s_setprio 0
	s_barrier
	s_add_i32 s57, s57, 2
	s_add_u32 s24, s24, 0x100
	s_addc_u32 s25, s25, 0
	s_add_u32 s49, s49, 0x100
	s_addc_u32 s56, s56, 0
	s_cmp_gt_u32 s57, 13

;     __device__ __forceinline__ void operator()(const f32x4 (&acc)[2][2][4][2], const Unit& u, int wr, int wc, int fr, int fq) const {
;         float xv[2][4];
;         {
;             f32x4 qd[2][4];
; #pragma unroll
;             for (int ai = 0; ai < 2; ++ai)
; #pragma unroll
;                 for (int m = 0; m < 4; ++m) qd[ai][m] = row_quad(ssq, u.pm * BM + ai * HALF + wr * 64 + m * 16 + fr, fq);
; #pragma unroll
;             for (int ai = 0; ai < 2; ++ai)
; #pragma unroll
;                 for (int m = 0; m < 4; ++m) asm volatile("" : "+v"(qd[ai][m]));
; #pragma unroll
;             for (int ai = 0; ai < 2; ++ai)
; #pragma unroll
;                 for (int m = 0; m < 4; ++m) xv[ai][m] = row_ms_from_quad(qd[ai][m], 1.0f / 1024.0f);
;         }
; #pragma unroll
;         for (int ai = 0; ai < 2; ++ai)
; #pragma unroll
;             for (int m = 0; m < 4; ++m) {
;                 const int row = u.pm * BM + ai * HALF + wr * 64 + m * 16 + fr;
;                 const float x = xv[ai][m], rs = __builtin_amdgcn_rsqf(x);
.LBB0_2815:
	v_lshl_add_u32 v162, s22, 8, v164
	v_or_b32_e32 v160, 16, v162
	v_or_b32_e32 v158, 32, v162
	v_or_b32_e32 v156, 48, v162
	v_add_u32_e32 v154, 0x80, v162
	v_add_u32_e32 v152, 0x90, v162
	v_add_u32_e32 v150, 0xa0, v162
	v_add_u32_e32 v148, 0xb0, v162
	v_and_b32_e32 v151, 64, v169
	v_xor_b32_e32 v149, 16, v169
	v_add_u32_e32 v151, 64, v151
	v_xor_b32_e32 v153, 32, v169
	v_cmp_lt_i32_e32 vcc, v149, v151
	v_mul_f32_e32 v120, v124, v120
	v_mul_f32_e32 v121, v125, v121
	v_cndmask_b32_e32 v149, v169, v149, vcc
	v_cmp_lt_i32_e32 vcc, v153, v151
	v_lshlrev_b32_e32 v149, 2, v149
	v_mul_f32_e32 v122, v126, v122
	v_cndmask_b32_e32 v151, v169, v153, vcc
	v_lshlrev_b32_e32 v151, 2, v151
	v_mul_f32_e32 v112, v116, v112
	v_mul_f32_e32 v113, v117, v113
	v_mul_f32_e32 v114, v118, v114
	s_lshl_b32 s22, s23, 7
	v_mul_f32_e32 v123, v127, v123
	s_ashr_i32 s23, s22, 31
	s_lshl_b64 s[22:23], s[22:23], 1
	v_mul_f32_e32 v104, v108, v104
	v_mul_f32_e32 v105, v109, v105
	v_mul_f32_e32 v106, v110, v106
	v_mul_f32_e32 v96, v100, v96
	v_mul_f32_e32 v97, v101, v97
	v_mul_f32_e32 v107, v111, v107
	v_mul_f32_e32 v98, v102, v98
	v_mul_f32_e32 v88, v92, v88
	v_mul_f32_e32 v89, v93, v89
	v_mul_f32_e32 v90, v94, v90
	v_mul_f32_e32 v80, v84, v80
	v_mul_f32_e32 v81, v85, v81
	v_mul_f32_e32 v91, v95, v91
	v_mul_f32_e32 v82, v86, v82
	v_mul_f32_e32 v72, v76, v72
	v_mul_f32_e32 v73, v77, v73
	v_mul_f32_e32 v74, v78, v74
	v_mul_f32_e32 v64, v68, v64
	v_mul_f32_e32 v65, v69, v65
	v_mul_f32_e32 v75, v79, v75
	v_mul_f32_e32 v66, v70, v66
	v_mul_f32_e32 v56, v60, v56
	v_mul_f32_e32 v57, v61, v57
	v_mul_f32_e32 v58, v62, v58
	v_mul_f32_e32 v48, v52, v48
	v_mul_f32_e32 v49, v53, v49
	v_mul_f32_e32 v59, v63, v59
	v_mul_f32_e32 v50, v54, v50
	v_mul_f32_e32 v40, v44, v40
	v_mul_f32_e32 v41, v45, v41
	v_mul_f32_e32 v42, v46, v42
	v_mul_f32_e32 v32, v36, v32
	v_mul_f32_e32 v33, v37, v33
	s_nop 0
	v_add_f32_e32 v153, v220, v221
	v_add_f32_e32 v153, v222, v153
	v_add_f32_e32 v155, v224, v225
	v_add_f32_e32 v153, v223, v153
	v_add_f32_e32 v155, v226, v155
	ds_bpermute_b32 v171, v149, v153
	v_add_f32_e32 v155, v227, v155
	ds_bpermute_b32 v172, v149, v155
	v_add_f32_e32 v157, v228, v229
	v_add_f32_e32 v157, v230, v157
	v_add_f32_e32 v159, v232, v233
	v_add_f32_e32 v159, v234, v159
	v_add_f32_e32 v157, v231, v157
	v_add_f32_e32 v159, v235, v159
	ds_bpermute_b32 v173, v149, v157
	ds_bpermute_b32 v174, v149, v159
	s_waitcnt lgkmcnt(3)
	v_add_f32_e32 v153, v153, v171
	ds_bpermute_b32 v171, v151, v153
	v_add_f32_e32 v161, v236, v237
	s_waitcnt lgkmcnt(3)
	v_add_f32_e32 v155, v155, v172
	v_add_f32_e32 v161, v238, v161
	ds_bpermute_b32 v172, v151, v155
	v_add_f32_e32 v161, v239, v161
	ds_bpermute_b32 v175, v149, v161
	s_waitcnt lgkmcnt(4)
	v_add_f32_e32 v157, v157, v173
	s_waitcnt lgkmcnt(3)
	v_add_f32_e32 v159, v159, v174
	ds_bpermute_b32 v173, v151, v157
	ds_bpermute_b32 v174, v151, v159
	v_add_f32_e32 v163, v240, v241
	s_waitcnt lgkmcnt(4)
	v_add_f32_e32 v153, v153, v171
	v_add_f32_e32 v163, v242, v163
	v_fmamk_f32 v171, v153, 0x3a800000, v170
	s_waitcnt lgkmcnt(3)
	v_add_f32_e32 v153, v155, v172
	v_add_f32_e32 v172, v244, v245
	v_add_f32_e32 v163, v243, v163
	v_add_f32_e32 v172, v246, v172
	ds_bpermute_b32 v176, v149, v163
	s_waitcnt lgkmcnt(3)
	v_add_f32_e32 v161, v161, v175
	v_add_f32_e32 v172, v247, v172
	ds_bpermute_b32 v175, v151, v161
	s_waitcnt lgkmcnt(3)
	v_add_f32_e32 v155, v157, v173
	ds_bpermute_b32 v173, v149, v172
	s_waitcnt lgkmcnt(3)
	v_add_f32_e32 v157, v159, v174
	v_add_f32_e32 v174, v248, v249
	v_add_f32_e32 v174, v250, v174
	v_add_f32_e32 v174, v251, v174
	s_waitcnt lgkmcnt(2)
	v_add_f32_e32 v163, v163, v176
	ds_bpermute_b32 v149, v149, v174
	s_waitcnt lgkmcnt(2)
	v_add_f32_e32 v159, v161, v175
	v_fmamk_f32 v161, v153, 0x3a800000, v170
	ds_bpermute_b32 v153, v151, v163
	s_waitcnt lgkmcnt(2)
	v_add_f32_e32 v172, v172, v173
	ds_bpermute_b32 v173, v151, v172
	s_waitcnt lgkmcnt(2)
	v_add_f32_e32 v149, v174, v149
	v_fmamk_f32 v155, v155, 0x3a800000, v170
	s_waitcnt lgkmcnt(1)
	v_add_f32_e32 v153, v163, v153
	ds_bpermute_b32 v163, v151, v149
	s_waitcnt lgkmcnt(1)
	v_add_f32_e32 v151, v172, v173
	v_rsq_f32_e32 v172, v171
	v_fmamk_f32 v157, v157, 0x3a800000, v170
	v_fmamk_f32 v159, v159, 0x3a800000, v170
	s_waitcnt lgkmcnt(0)
; __device__ __forceinline__ unsigned cvt_pk_bf16(float lo, float hi) { unsigned r; asm volatile("v_cvt_pk_bf16_f32 %0, %1, %2" : "=v"(r) : "v"(lo), "v"(hi)); return r; }
;     __device__ __forceinline__ void operator()(const f32x4 (&acc)[2][2][4][2], const Unit& u, int wr, int wc, int fr, int fq) const {
;     ...
;             for (int m = 0; m < 4; ++m) {
;                 const int row = u.pm * BM + ai * HALF + wr * 64 + m * 16 + fr;
;                 const float x = xv[ai][m], rs = __builtin_amdgcn_rsqf(x);
;                 const float ea = -1.4426950408889634f * rs;
;                 float h[8];
; #pragma unroll
;                 for (int n = 0; n < 2; ++n)
; #pragma unroll
;                     for (int j = 0; j < 4; ++j) {
;                         const float g = acc[ai][0][m][n][j], uu = acc[ai][1][m][n][j];
;                         const float e = __builtin_amdgcn_exp2f(g * ea);
;                         const float q = __builtin_amdgcn_rcpf(__builtin_fmaf(e, x, x));
;                         h[n * 4 + j] = (g * uu) * q;
;                     }
;                 u32x4 w; w.x = cvt_pk_bf16(h[0], h[1]); w.y = cvt_pk_bf16(h[2], h[3]); w.z = cvt_pk_bf16(h[4], h[5]); w.w = cvt_pk_bf16(h[6], h[7]);
;                 *(u32x4*)(Hd + (size_t)row * ldh + u.pn * HALF + wc * 32 + 8 * fq) = w;
	v_add_f32_e32 v149, v149, v163
	v_mul_f32_e32 v163, 0xbfb8aa3b, v172
	v_mul_f32_e32 v173, v125, v163
	v_exp_f32_e32 v173, v173
	v_mul_f32_e32 v172, v124, v163
	v_exp_f32_e32 v172, v172
	v_mul_f32_e32 v125, v127, v163
	v_fma_f32 v124, v173, v171, v171
	v_mul_f32_e32 v173, v126, v163
	v_rcp_f32_e32 v124, v124
	v_exp_f32_e32 v173, v173
	v_mul_f32_e32 v126, v117, v163
	v_exp_f32_e32 v126, v126
	v_mul_f32_e32 v121, v121, v124
	v_fma_f32 v124, v173, v171, v171
	v_rcp_f32_e32 v124, v124
	v_mul_f32_e32 v117, v118, v163
	v_exp_f32_e32 v117, v117
	v_exp_f32_e32 v125, v125
	v_mul_f32_e32 v122, v122, v124
	v_mul_f32_e32 v124, v116, v163
	v_exp_f32_e32 v124, v124
	v_fma_f32 v116, v126, v171, v171
	v_rcp_f32_e32 v116, v116
	v_fma_f32 v172, v172, v171, v171
	v_fma_f32 v124, v124, v171, v171
	v_rcp_f32_e32 v124, v124
	v_mul_f32_e32 v113, v113, v116
	v_fma_f32 v116, v117, v171, v171
	v_rcp_f32_e32 v172, v172
	v_mul_f32_e32 v112, v112, v124
	v_mul_f32_e32 v124, v119, v163
	v_exp_f32_e32 v124, v124
	v_fma_f32 v125, v125, v171, v171
	v_rcp_f32_e32 v116, v116
	v_rcp_f32_e32 v125, v125
	v_fmac_f32_e32 v171, v124, v171
	v_rcp_f32_e32 v117, v171
	v_mul_f32_e32 v120, v120, v172
	v_mul_f32_e32 v118, v114, v116
	v_mul_f32_e32 v114, v119, v115
	v_mul_f32_e32 v123, v123, v125
	v_mul_f32_e32 v117, v114, v117
	v_cvt_pk_bf16_f32 v114, v120, v121
	v_cvt_pk_bf16_f32 v115, v122, v123
	v_cvt_pk_bf16_f32 v116, v112, v113
	v_mov_b64_e32 v[112:113], s[8:9]
	v_rsq_f32_e32 v120, v161
	v_cvt_pk_bf16_f32 v117, v118, v117
	v_mad_i64_i32 v[118:119], s[24:25], v162, s45, v[112:113]
	v_lshl_add_u64 v[118:119], v[118:119], 0, s[22:23]
	v_lshl_add_u64 v[118:119], v[118:119], 0, s[4:5]
	v_lshl_add_u64 v[118:119], v[118:119], 0, v[136:137]
	v_mul_f32_e32 v120, 0xbfb8aa3b, v120
	global_store_dwordx4 v[118:119], v[114:117], off
	v_mul_f32_e32 v121, v108, v120
	v_exp_f32_e32 v121, v121
	v_mul_f32_e32 v114, v109, v120
	v_exp_f32_e32 v114, v114
	v_mul_f32_e32 v109, v111, v120
	v_exp_f32_e32 v109, v109
	v_fma_f32 v115, v121, v161, v161
	v_fma_f32 v108, v114, v161, v161
	v_mul_f32_e32 v114, v110, v120
	v_rcp_f32_e32 v108, v108
	v_exp_f32_e32 v114, v114
	v_mul_f32_e32 v110, v101, v120
	v_exp_f32_e32 v110, v110
	v_mul_f32_e32 v105, v105, v108
	v_fma_f32 v108, v114, v161, v161
	v_rcp_f32_e32 v108, v108
	v_fma_f32 v109, v109, v161, v161
	v_mul_f32_e32 v101, v102, v120
	v_rcp_f32_e32 v109, v109
	v_mul_f32_e32 v106, v106, v108
	v_mul_f32_e32 v108, v100, v120
	v_exp_f32_e32 v108, v108
	v_exp_f32_e32 v101, v101
	v_mul_f32_e32 v107, v107, v109
	v_rcp_f32_e32 v115, v115
	v_fma_f32 v108, v108, v161, v161
	v_rcp_f32_e32 v108, v108
	v_rsq_f32_e32 v102, v155
	v_mul_f32_e32 v104, v104, v115
	v_fmamk_f32 v153, v153, 0x3a800000, v170
	v_mul_f32_e32 v100, v96, v108
	v_fma_f32 v96, v110, v161, v161
	v_rcp_f32_e32 v96, v96
	v_mul_f32_e32 v108, v103, v120
	v_exp_f32_e32 v108, v108
	v_mul_f32_e32 v102, 0xbfb8aa3b, v102
	v_mul_f32_e32 v109, v97, v96
	v_fma_f32 v96, v101, v161, v161
	v_rcp_f32_e32 v96, v96
	v_fmac_f32_e32 v161, v108, v161
	v_rcp_f32_e32 v97, v161
	v_mul_f32_e32 v43, v47, v43
	v_mul_f32_e32 v101, v98, v96
	v_mul_f32_e32 v96, v103, v99
	v_mul_f32_e32 v99, v96, v97
	v_cvt_pk_bf16_f32 v96, v104, v105
	v_cvt_pk_bf16_f32 v97, v106, v107
	v_cvt_pk_bf16_f32 v98, v100, v109
	v_cvt_pk_bf16_f32 v99, v101, v99
	v_mad_i64_i32 v[100:101], s[24:25], v160, s45, v[112:113]
	v_lshl_add_u64 v[100:101], v[100:101], 0, s[22:23]
	v_lshl_add_u64 v[100:101], v[100:101], 0, s[4:5]
	v_lshl_add_u64 v[100:101], v[100:101], 0, v[136:137]
	global_store_dwordx4 v[100:101], v[96:99], off
	v_mul_f32_e32 v103, v92, v102
	v_exp_f32_e32 v103, v103
	v_mul_f32_e32 v96, v93, v102
	v_exp_f32_e32 v96, v96
	v_mul_f32_e32 v93, v95, v102
	v_exp_f32_e32 v93, v93
	v_fma_f32 v97, v103, v155, v155
	v_fma_f32 v92, v96, v155, v155
	v_mul_f32_e32 v96, v94, v102
	v_rcp_f32_e32 v92, v92
	v_exp_f32_e32 v96, v96
	v_mul_f32_e32 v94, v85, v102
	v_exp_f32_e32 v94, v94
	v_mul_f32_e32 v89, v89, v92
	v_fma_f32 v92, v96, v155, v155
	v_rcp_f32_e32 v92, v92
	v_fma_f32 v93, v93, v155, v155
	v_mul_f32_e32 v85, v86, v102
	v_rcp_f32_e32 v93, v93
	v_mul_f32_e32 v90, v90, v92
	v_mul_f32_e32 v92, v84, v102
	v_exp_f32_e32 v92, v92
	v_exp_f32_e32 v85, v85
	v_mul_f32_e32 v91, v91, v93
	v_rcp_f32_e32 v97, v97
	v_fma_f32 v92, v92, v155, v155
	v_rcp_f32_e32 v92, v92
	v_rsq_f32_e32 v86, v157
	v_mul_f32_e32 v88, v88, v97
	v_mul_f32_e32 v34, v38, v34
	v_mul_f32_e32 v84, v80, v92
	v_fma_f32 v80, v94, v155, v155
	v_rcp_f32_e32 v80, v80
	v_mul_f32_e32 v92, v87, v102
	v_exp_f32_e32 v92, v92
	v_mul_f32_e32 v86, 0xbfb8aa3b, v86
	v_mul_f32_e32 v93, v81, v80
	v_fma_f32 v80, v85, v155, v155
	v_rcp_f32_e32 v80, v80
	v_fmac_f32_e32 v155, v92, v155
	v_rcp_f32_e32 v81, v155
	v_fmamk_f32 v151, v151, 0x3a800000, v170
	v_mul_f32_e32 v85, v82, v80
	v_mul_f32_e32 v80, v87, v83
	v_mul_f32_e32 v83, v80, v81
	v_cvt_pk_bf16_f32 v80, v88, v89
	v_cvt_pk_bf16_f32 v81, v90, v91
	v_cvt_pk_bf16_f32 v82, v84, v93
	v_cvt_pk_bf16_f32 v83, v85, v83
	v_mad_i64_i32 v[84:85], s[24:25], v158, s45, v[112:113]
	v_lshl_add_u64 v[84:85], v[84:85], 0, s[22:23]
	v_lshl_add_u64 v[84:85], v[84:85], 0, s[4:5]
	v_lshl_add_u64 v[84:85], v[84:85], 0, v[136:137]
	global_store_dwordx4 v[84:85], v[80:83], off
	v_mul_f32_e32 v87, v76, v86
	v_exp_f32_e32 v87, v87
	v_mul_f32_e32 v80, v77, v86
	v_exp_f32_e32 v80, v80
	v_mul_f32_e32 v77, v79, v86
	v_exp_f32_e32 v77, v77
	v_fma_f32 v81, v87, v157, v157
	v_fma_f32 v76, v80, v157, v157
	v_mul_f32_e32 v80, v78, v86
	v_rcp_f32_e32 v76, v76
	v_exp_f32_e32 v80, v80
	v_mul_f32_e32 v78, v69, v86
	v_exp_f32_e32 v78, v78
	v_mul_f32_e32 v73, v73, v76
	v_fma_f32 v76, v80, v157, v157
; __device__ __forceinline__ unsigned cvt_pk_bf16(float lo, float hi) { unsigned r; asm volatile("v_cvt_pk_bf16_f32 %0, %1, %2" : "=v"(r) : "v"(lo), "v"(hi)); return r; }
;     __device__ __forceinline__ void operator()(const f32x4 (&acc)[2][2][4][2], const Unit& u, int wr, int wc, int fr, int fq) const {
;     ...
;                 const int row = u.pm * BM + ai * HALF + wr * 64 + m * 16 + fr;
;                 const float x = xv[ai][m], rs = __builtin_amdgcn_rsqf(x);
;                 const float ea = -1.4426950408889634f * rs;
;                 float h[8];
; #pragma unroll
;                 for (int n = 0; n < 2; ++n)
; #pragma unroll
;                     for (int j = 0; j < 4; ++j) {
;                         const float g = acc[ai][0][m][n][j], uu = acc[ai][1][m][n][j];
;                         const float e = __builtin_amdgcn_exp2f(g * ea);
;                         const float q = __builtin_amdgcn_rcpf(__builtin_fmaf(e, x, x));
;                         h[n * 4 + j] = (g * uu) * q;
;                     }
;                 u32x4 w; w.x = cvt_pk_bf16(h[0], h[1]); w.y = cvt_pk_bf16(h[2], h[3]); w.z = cvt_pk_bf16(h[4], h[5]); w.w = cvt_pk_bf16(h[6], h[7]);
;                 *(u32x4*)(Hd + (size_t)row * ldh + u.pn * HALF + wc * 32 + 8 * fq) = w;
	v_rcp_f32_e32 v76, v76
	v_fma_f32 v77, v77, v157, v157
	v_mul_f32_e32 v69, v70, v86
	v_rcp_f32_e32 v77, v77
	v_mul_f32_e32 v74, v74, v76
	v_mul_f32_e32 v76, v68, v86
	v_exp_f32_e32 v76, v76
	v_exp_f32_e32 v69, v69
	v_mul_f32_e32 v75, v75, v77
	v_rcp_f32_e32 v81, v81
	v_fma_f32 v76, v76, v157, v157
	v_rcp_f32_e32 v76, v76
	v_rsq_f32_e32 v70, v159
	v_mul_f32_e32 v72, v72, v81
	v_mul_f32_e32 v24, v28, v24
	v_mul_f32_e32 v68, v64, v76
	v_fma_f32 v64, v78, v157, v157
	v_rcp_f32_e32 v64, v64
	v_mul_f32_e32 v76, v71, v86
	v_exp_f32_e32 v76, v76
	v_mul_f32_e32 v70, 0xbfb8aa3b, v70
	v_mul_f32_e32 v77, v65, v64
	v_fma_f32 v64, v69, v157, v157
	v_rcp_f32_e32 v64, v64
	v_fmac_f32_e32 v157, v76, v157
	v_rcp_f32_e32 v65, v157
	v_mul_f32_e32 v25, v29, v25
	v_mul_f32_e32 v69, v66, v64
	v_mul_f32_e32 v64, v71, v67
	v_mul_f32_e32 v67, v64, v65
	v_cvt_pk_bf16_f32 v64, v72, v73
	v_cvt_pk_bf16_f32 v65, v74, v75
	v_cvt_pk_bf16_f32 v66, v68, v77
	v_cvt_pk_bf16_f32 v67, v69, v67
	v_mad_i64_i32 v[68:69], s[24:25], v156, s45, v[112:113]
	v_lshl_add_u64 v[68:69], v[68:69], 0, s[22:23]
	v_lshl_add_u64 v[68:69], v[68:69], 0, s[4:5]
	v_lshl_add_u64 v[68:69], v[68:69], 0, v[136:137]
	global_store_dwordx4 v[68:69], v[64:67], off
	v_mul_f32_e32 v71, v60, v70
	v_exp_f32_e32 v71, v71
	v_mul_f32_e32 v64, v61, v70
	v_exp_f32_e32 v64, v64
	v_mul_f32_e32 v61, v63, v70
	v_exp_f32_e32 v61, v61
	v_fma_f32 v65, v71, v159, v159
	v_fma_f32 v60, v64, v159, v159
	v_mul_f32_e32 v64, v62, v70
	v_rcp_f32_e32 v60, v60
	v_exp_f32_e32 v64, v64
	v_mul_f32_e32 v62, v53, v70
	v_exp_f32_e32 v62, v62
	v_mul_f32_e32 v57, v57, v60
	v_fma_f32 v60, v64, v159, v159
	v_rcp_f32_e32 v60, v60
	v_fma_f32 v61, v61, v159, v159
	v_mul_f32_e32 v53, v54, v70
	v_rcp_f32_e32 v61, v61
	v_mul_f32_e32 v58, v58, v60
	v_mul_f32_e32 v60, v52, v70
	v_exp_f32_e32 v60, v60
	v_exp_f32_e32 v53, v53
	v_mul_f32_e32 v59, v59, v61
	v_rcp_f32_e32 v65, v65
	v_fma_f32 v60, v60, v159, v159
	v_rcp_f32_e32 v60, v60
	v_rsq_f32_e32 v54, v153
	v_mul_f32_e32 v56, v56, v65
	v_mul_f32_e32 v26, v30, v26
	v_mul_f32_e32 v52, v48, v60
	v_fma_f32 v48, v62, v159, v159
	v_rcp_f32_e32 v48, v48
	v_mul_f32_e32 v60, v55, v70
	v_exp_f32_e32 v60, v60
	v_mul_f32_e32 v54, 0xbfb8aa3b, v54
	v_mul_f32_e32 v61, v49, v48
	v_fma_f32 v48, v53, v159, v159
	v_rcp_f32_e32 v48, v48
	v_fmac_f32_e32 v159, v60, v159
	v_rcp_f32_e32 v49, v159
	v_mul_f32_e32 v16, v20, v16
	v_mul_f32_e32 v53, v50, v48
	v_mul_f32_e32 v48, v55, v51
	v_mul_f32_e32 v51, v48, v49
	v_cvt_pk_bf16_f32 v48, v56, v57
	v_cvt_pk_bf16_f32 v49, v58, v59
	v_cvt_pk_bf16_f32 v50, v52, v61
	v_cvt_pk_bf16_f32 v51, v53, v51
	v_mad_i64_i32 v[52:53], s[24:25], v154, s45, v[112:113]
	v_lshl_add_u64 v[52:53], v[52:53], 0, s[22:23]
	v_lshl_add_u64 v[52:53], v[52:53], 0, s[4:5]
	v_lshl_add_u64 v[52:53], v[52:53], 0, v[136:137]
	global_store_dwordx4 v[52:53], v[48:51], off
	v_mul_f32_e32 v55, v44, v54
	v_exp_f32_e32 v55, v55
	v_mul_f32_e32 v48, v45, v54
	v_exp_f32_e32 v48, v48
	v_mul_f32_e32 v45, v47, v54
	v_exp_f32_e32 v45, v45
	v_fma_f32 v49, v55, v153, v153
	v_fma_f32 v44, v48, v153, v153
	v_mul_f32_e32 v48, v46, v54
	v_rcp_f32_e32 v44, v44
	v_exp_f32_e32 v48, v48
	v_mul_f32_e32 v46, v37, v54
	v_exp_f32_e32 v46, v46
	v_mul_f32_e32 v41, v41, v44
	v_fma_f32 v44, v48, v153, v153
	v_rcp_f32_e32 v44, v44
	v_fma_f32 v45, v45, v153, v153
	v_mul_f32_e32 v37, v38, v54
	v_rcp_f32_e32 v45, v45
	v_mul_f32_e32 v42, v42, v44
	v_mul_f32_e32 v44, v36, v54
	v_exp_f32_e32 v44, v44
	v_exp_f32_e32 v37, v37
	v_mul_f32_e32 v43, v43, v45
	v_rcp_f32_e32 v49, v49
	v_fma_f32 v44, v44, v153, v153
	v_rcp_f32_e32 v44, v44
	v_rsq_f32_e32 v38, v151
	v_mul_f32_e32 v40, v40, v49
	v_mul_f32_e32 v17, v21, v17
	v_mul_f32_e32 v36, v32, v44
	v_fma_f32 v32, v46, v153, v153
	v_rcp_f32_e32 v32, v32
	v_mul_f32_e32 v44, v39, v54
	v_exp_f32_e32 v44, v44
	v_mul_f32_e32 v38, 0xbfb8aa3b, v38
	v_mul_f32_e32 v45, v33, v32
	v_fma_f32 v32, v37, v153, v153
	v_rcp_f32_e32 v32, v32
	v_fmac_f32_e32 v153, v44, v153
; __device__ __forceinline__ unsigned cvt_pk_bf16(float lo, float hi) { unsigned r; asm volatile("v_cvt_pk_bf16_f32 %0, %1, %2" : "=v"(r) : "v"(lo), "v"(hi)); return r; }
; #define PG8_BAR __builtin_amdgcn_s_barrier()
;     __device__ __forceinline__ void operator()(const f32x4 (&acc)[2][2][4][2], const Unit& u, int wr, int wc, int fr, int fq) const {
;     ...
;                 const int row = u.pm * BM + ai * HALF + wr * 64 + m * 16 + fr;
;                 const float x = xv[ai][m], rs = __builtin_amdgcn_rsqf(x);
;                 const float ea = -1.4426950408889634f * rs;
;                 float h[8];
; #pragma unroll
;                 for (int n = 0; n < 2; ++n)
; #pragma unroll
;                     for (int j = 0; j < 4; ++j) {
;                         const float g = acc[ai][0][m][n][j], uu = acc[ai][1][m][n][j];
;                         const float e = __builtin_amdgcn_exp2f(g * ea);
;                         const float q = __builtin_amdgcn_rcpf(__builtin_fmaf(e, x, x));
;                         h[n * 4 + j] = (g * uu) * q;
;                     }
;                 u32x4 w; w.x = cvt_pk_bf16(h[0], h[1]); w.y = cvt_pk_bf16(h[2], h[3]); w.z = cvt_pk_bf16(h[4], h[5]); w.w = cvt_pk_bf16(h[6], h[7]);
;                 *(u32x4*)(Hd + (size_t)row * ldh + u.pn * HALF + wc * 32 + 8 * fq) = w;
; template <class Epi, class Sched, bool ALIGN_EPI = false, bool SP2 = false>
; __device__ __forceinline__ void gemm_phase(PG8_LAS unsigned char* lds, const Gemm g, const Sched& S, const Epi& E, const int wid) {
;     ...
;         if (!has_next) break;
; #pragma unroll
;         for (int a = 0; a < 2; ++a)
; #pragma unroll
;             for (int b = 0; b < 2; ++b)
; #pragma unroll
;                 for (int m = 0; m < 4; ++m)
; #pragma unroll
;                     for (int n = 0; n < 2; ++n) acc[a][b][m][n] = (f32x4){0.f, 0.f, 0.f, 0.f};
;         cur = nxt; cA = nA; cB = nB; ++ui;
;         if constexpr (ALIGN_EPI) { if (wr == 1) PG8_BAR; }
	v_rcp_f32_e32 v33, v153
	v_mul_f32_e32 v27, v31, v27
	v_mul_f32_e32 v37, v34, v32
	v_mul_f32_e32 v32, v39, v35
	v_mul_f32_e32 v35, v32, v33
	v_cvt_pk_bf16_f32 v32, v40, v41
	v_cvt_pk_bf16_f32 v33, v42, v43
	v_cvt_pk_bf16_f32 v34, v36, v45
	v_cvt_pk_bf16_f32 v35, v37, v35
	v_mad_i64_i32 v[36:37], s[24:25], v152, s45, v[112:113]
	v_lshl_add_u64 v[36:37], v[36:37], 0, s[22:23]
	v_lshl_add_u64 v[36:37], v[36:37], 0, s[4:5]
	v_lshl_add_u64 v[36:37], v[36:37], 0, v[136:137]
	global_store_dwordx4 v[36:37], v[32:35], off
	v_mul_f32_e32 v39, v28, v38
	v_exp_f32_e32 v39, v39
	v_mul_f32_e32 v32, v29, v38
	v_exp_f32_e32 v32, v32
	v_mul_f32_e32 v29, v31, v38
	v_exp_f32_e32 v29, v29
	v_fma_f32 v33, v39, v151, v151
	v_fma_f32 v28, v32, v151, v151
	v_mul_f32_e32 v32, v30, v38
	v_rcp_f32_e32 v28, v28
	v_exp_f32_e32 v32, v32
	v_mul_f32_e32 v30, v21, v38
	v_exp_f32_e32 v30, v30
	v_mul_f32_e32 v25, v25, v28
	v_fma_f32 v28, v32, v151, v151
	v_rcp_f32_e32 v28, v28
	v_fma_f32 v29, v29, v151, v151
	v_mul_f32_e32 v21, v22, v38
	v_rcp_f32_e32 v29, v29
	v_mul_f32_e32 v26, v26, v28
	v_mul_f32_e32 v28, v20, v38
	v_exp_f32_e32 v28, v28
	v_exp_f32_e32 v21, v21
	v_mul_f32_e32 v27, v27, v29
	v_rcp_f32_e32 v33, v33
	v_fma_f32 v28, v28, v151, v151
	v_rcp_f32_e32 v28, v28
	v_mul_f32_e32 v18, v22, v18
	v_fmamk_f32 v149, v149, 0x3a800000, v170
	v_rsq_f32_e32 v22, v149
	v_mul_f32_e32 v20, v16, v28
	v_fma_f32 v16, v30, v151, v151
	v_rcp_f32_e32 v16, v16
	v_mul_f32_e32 v28, v23, v38
	v_exp_f32_e32 v28, v28
	v_mul_f32_e32 v24, v24, v33
	v_mul_f32_e32 v29, v17, v16
	v_fma_f32 v16, v21, v151, v151
	v_rcp_f32_e32 v16, v16
	v_fmac_f32_e32 v151, v28, v151
	v_rcp_f32_e32 v17, v151
	v_mul_f32_e32 v22, 0xbfb8aa3b, v22
	v_mul_f32_e32 v21, v18, v16
	v_mul_f32_e32 v16, v23, v19
	v_mul_f32_e32 v19, v16, v17
	v_cvt_pk_bf16_f32 v16, v24, v25
	v_cvt_pk_bf16_f32 v17, v26, v27
	v_cvt_pk_bf16_f32 v18, v20, v29
	v_cvt_pk_bf16_f32 v19, v21, v19
	v_mad_i64_i32 v[20:21], s[24:25], v150, s45, v[112:113]
	v_lshl_add_u64 v[20:21], v[20:21], 0, s[22:23]
	v_lshl_add_u64 v[20:21], v[20:21], 0, s[4:5]
	v_lshl_add_u64 v[20:21], v[20:21], 0, v[136:137]
	global_store_dwordx4 v[20:21], v[16:19], off
	v_mul_f32_e32 v23, v12, v22
	v_mul_f32_e32 v8, v12, v8
	v_mul_f32_e32 v16, v13, v22
	v_exp_f32_e32 v16, v16
	v_mul_f32_e32 v9, v13, v9
	v_mul_f32_e32 v10, v14, v10
	v_mul_f32_e32 v13, v15, v22
	v_fma_f32 v12, v16, v149, v149
	v_mul_f32_e32 v16, v14, v22
	v_rcp_f32_e32 v12, v12
	v_exp_f32_e32 v16, v16
	v_mul_f32_e32 v14, v5, v22
	v_exp_f32_e32 v13, v13
	v_mul_f32_e32 v9, v9, v12
	v_fma_f32 v12, v16, v149, v149
	v_rcp_f32_e32 v12, v12
	v_exp_f32_e32 v14, v14
	v_mul_f32_e32 v0, v4, v0
	v_fma_f32 v13, v13, v149, v149
	v_mul_f32_e32 v10, v10, v12
	v_mul_f32_e32 v12, v4, v22
	v_exp_f32_e32 v12, v12
	v_mul_f32_e32 v1, v5, v1
	v_mul_f32_e32 v5, v6, v22
	v_rcp_f32_e32 v13, v13
	v_fma_f32 v12, v12, v149, v149
	v_rcp_f32_e32 v12, v12
	v_exp_f32_e32 v5, v5
	v_exp_f32_e32 v23, v23
	v_mul_f32_e32 v11, v15, v11
	v_mul_f32_e32 v4, v0, v12
	v_fma_f32 v0, v14, v149, v149
	v_rcp_f32_e32 v0, v0
	v_mul_f32_e32 v12, v7, v22
	v_exp_f32_e32 v12, v12
	v_mul_f32_e32 v11, v11, v13
	v_mul_f32_e32 v13, v1, v0
	v_fma_f32 v0, v5, v149, v149
	v_fma_f32 v17, v23, v149, v149
	v_rcp_f32_e32 v0, v0
	v_fmac_f32_e32 v149, v12, v149
	v_rcp_f32_e32 v1, v149
	v_rcp_f32_e32 v17, v17
	v_mul_f32_e32 v2, v6, v2
	v_mul_f32_e32 v5, v2, v0
	v_mul_f32_e32 v0, v7, v3
	v_mul_f32_e32 v3, v0, v1
	v_mul_f32_e32 v8, v8, v17
	v_cvt_pk_bf16_f32 v0, v8, v9
	v_cvt_pk_bf16_f32 v1, v10, v11
	v_cvt_pk_bf16_f32 v2, v4, v13
	v_cvt_pk_bf16_f32 v3, v5, v3
	v_mad_i64_i32 v[4:5], s[24:25], v148, s45, v[112:113]
	v_lshl_add_u64 v[4:5], v[4:5], 0, s[22:23]
	v_lshl_add_u64 v[4:5], v[4:5], 0, s[4:5]
	v_lshl_add_u64 v[4:5], v[4:5], 0, v[136:137]
	s_andn2_b64 vcc, exec, s[2:3]
	s_mov_b64 s[2:3], -1
	global_store_dwordx4 v[4:5], v[0:3], off
	s_cbranch_vccnz .LBB0_2808
	s_andn2_b64 vcc, exec, s[6:7]
	s_cbranch_vccnz .LBB0_2807
	s_barrier
	s_branch .LBB0_2807
